# attention: two query tiles per wave interleaved with shared K/V^T fragments, conflict-free V^T tile, earlier staging/query loads (on top of v33)
# speedup vs baseline: 1.0141x; 1.0013x over previous
.LBB0_1396:
	s_or_b64 exec, exec, s[6:7]
	s_add_u32 s14, s12, 0x18000000
	s_addc_u32 s15, s13, 0
	s_add_u32 s16, s12, 0x2a000000
	s_addc_u32 s17, s13, 0
	s_add_u32 s30, s12, 0x22000000
	s_addc_u32 s31, s13, 0
	v_readfirstlane_b32 s33, v0
	v_and_b32_e32 v2, 15, v242
	v_lshrrev_b32_e32 v3, 4, v242
	s_lshr_b32 s33, s33, 6
	v_lshrrev_b32_e32 v232, 1, v0
	v_and_b32_e32 v233, 1, v0
	v_mul_u32_u24_e32 v4, 0x90, v232
	v_lshl_add_u32 v4, v233, 6, v4
	v_mul_u32_u24_e32 v6, 0x1400, v232
	v_lshl_add_u32 v6, v233, 6, v6
	v_lshlrev_b32_e32 v234, 7, v233
	v_add_u32_e32 v19, 0x15400, v234
	v_lshrrev_b32_e32 v232, 3, v0
	v_and_b32_e32 v233, 7, v0
	v_mul_u32_u24_e32 v5, 0x210, v232
	v_lshl_add_u32 v5, v233, 4, v5
	v_add_u32_e32 v5, 0x9000, v5
	v_lshlrev_b32_e32 v7, 15, v232
	v_lshl_add_u32 v7, v233, 4, v7
	v_mul_u32_u24_e32 v8, 0x1400, v2
	v_lshl_add_u32 v8, v3, 4, v8
	v_lshlrev_b32_e32 v9, 12, v2
	v_lshl_add_u32 v9, v3, 3, v9
	v_mul_u32_u24_e32 v10, 0x90, v2
	v_lshl_add_u32 v10, v3, 4, v10
	v_mul_u32_u24_e32 v11, 0x210, v2
	v_bfe_u32 v232, v2, 3, 1
	v_xor_b32_e32 v232, v232, v3
	v_lshl_add_u32 v11, v232, 3, v11
	v_add_u32_e32 v11, 0x9000, v11
	v_add_u32_e32 v12, 0x2100, v11
	v_add_u32_e32 v13, 0x4200, v11
	v_add_u32_e32 v14, 0x6300, v11
	v_xor_b32_e32 v15, 16, v242
	v_lshlrev_b32_e32 v15, 2, v15
	v_xor_b32_e32 v16, 32, v242
	v_lshlrev_b32_e32 v16, 2, v16
	v_xor_b32_e32 v17, 1, v242
	v_lshlrev_b32_e32 v17, 2, v17
	v_lshlrev_b32_e32 v232, 2, v3
	v_sub_u32_e32 v18, v2, v232
	v_add_u32_e32 v18, 0x80, v18
	v_mov_b32_e32 v89, 0xff800000
	v_mov_b32_e32 v90, 0
	v_mov_b32_e32 v144, 0
	v_mov_b32_e32 v145, 0
	s_mov_b32 s34, s96
	s_mov_b32 s55, -1
	s_waitcnt lgkmcnt(0)
	s_barrier
	s_cmpk_gt_u32 s34, 0x3ff
	s_cbranch_scc1 .Lat_done
	s_and_b32 s3, s34, 3
	s_bfe_u32 s4, s34, 0x70002
	s_lshr_b32 s5, s34, 9
	s_lshl_b32 s6, s5, 14
	s_lshl_b32 s7, s4, 7
	s_add_i32 s6, s6, s7
	s_sub_i32 s6, s6, 0x80
	s_mul_i32 s7, s6, 0x1400
	s_ashr_i32 s9, s7, 31
	s_add_u32 s40, s14, s7
	s_addc_u32 s41, s15, s9
	s_lshl_b32 s7, s3, 7
	s_add_u32 s40, s40, s7
	s_addc_u32 s41, s41, 0
	s_lshl_b32 s6, s5, 2
	s_add_i32 s6, s6, s3
	s_lshl_b32 s6, s6, 21
	s_lshl_b32 s7, s4, 8
	s_sub_i32 s7, s7, 0x100
	s_add_i32 s6, s6, s7
	s_ashr_i32 s7, s6, 31
	s_add_u32 s42, s16, s6
	s_addc_u32 s43, s17, s7
	global_load_dwordx4 v[92:95], v6, s[40:41] offset:0
	global_load_dwordx4 v[96:99], v6, s[40:41] offset:16
	global_load_dwordx4 v[100:103], v6, s[40:41] offset:32
	global_load_dwordx4 v[104:107], v6, s[40:41] offset:48
	global_load_dwordx4 v[112:115], v7, s[42:43] offset:0
	global_load_dwordx4 v[120:123], v7, s[42:43] offset:128
	global_load_dwordx4 v[128:131], v7, s[42:43] offset:256
	global_load_dwordx4 v[136:139], v7, s[42:43] offset:384
.Lat_item:
	s_and_b32 s35, s34, 3
	s_bfe_u32 s36, s34, 0x70002
	s_lshr_b32 s37, s34, 9
	s_lshl_b32 s38, s35, 3
	s_add_i32 s38, s38, s33
	s_lshl_b32 s2, s37, 14
	s_lshl_b32 s3, s36, 7
	s_add_i32 s2, s2, s3
	s_mul_hi_u32 s5, s2, 0x1400
	s_mul_i32 s4, s2, 0x1400
	s_add_u32 s48, s14, s4
	s_addc_u32 s49, s15, s5
	s_lshl_b32 s4, s38, 7
	s_add_i32 s4, s4, 0x400
	s_add_u32 s48, s48, s4
	s_addc_u32 s49, s49, 0
	s_lshr_b32 s5, s2, 20
	s_lshl_b32 s4, s2, 12
	s_add_u32 s50, s30, s4
	s_addc_u32 s51, s31, s5
	s_lshl_b32 s4, s38, 7
	s_add_u32 s50, s50, s4
	s_addc_u32 s51, s51, 0
	s_add_u32 s58, s48, 0x14000
	s_addc_u32 s59, s49, 0
	s_add_u32 s60, s50, 0x10000
	s_addc_u32 s61, s51, 0
	global_load_dwordx4 v[184:187], v8, s[48:49]
	global_load_dwordx4 v[188:191], v8, s[48:49] offset:64
	global_load_dwordx4 v[192:195], v8, s[58:59]
	global_load_dwordx4 v[196:199], v8, s[58:59] offset:64
	ds_read_b128 v[148:151], v19 offset:0
	ds_read_b128 v[152:155], v19 offset:16
	ds_read_b128 v[156:159], v19 offset:32
	ds_read_b128 v[160:163], v19 offset:48
	ds_read_b128 v[164:167], v19 offset:64
	ds_read_b128 v[168:171], v19 offset:80
	ds_read_b128 v[172:175], v19 offset:96
	ds_read_b128 v[176:179], v19 offset:112
	s_waitcnt vmcnt(4)
	s_cmp_lg_u32 s36, 0
	s_cbranch_scc1 .Lat_nz
	s_mov_b64 s[2:3], exec
	v_cmp_gt_u32_e32 vcc, 0x100, v0
	s_and_b64 exec, exec, vcc
	v_mov_b32_e32 v92, 0
	v_mov_b32_e32 v93, 0
	v_mov_b32_e32 v94, 0
	v_mov_b32_e32 v95, 0
	v_mov_b32_e32 v96, 0
	v_mov_b32_e32 v97, 0
	v_mov_b32_e32 v98, 0
	v_mov_b32_e32 v99, 0
	v_mov_b32_e32 v100, 0
	v_mov_b32_e32 v101, 0
	v_mov_b32_e32 v102, 0
	v_mov_b32_e32 v103, 0
	v_mov_b32_e32 v104, 0
	v_mov_b32_e32 v105, 0
	v_mov_b32_e32 v106, 0
	v_mov_b32_e32 v107, 0
	s_mov_b64 exec, s[2:3]
	v_mov_b32_e32 v112, 0
	v_mov_b32_e32 v113, 0
	v_mov_b32_e32 v114, 0
	v_mov_b32_e32 v115, 0
	v_mov_b32_e32 v120, 0
	v_mov_b32_e32 v121, 0
	v_mov_b32_e32 v122, 0
	v_mov_b32_e32 v123, 0
.Lat_nz:
	v_lshlrev_b32_e32 v20, 16, v92
	v_and_b32_e32 v21, 0xffff0000, v92
	v_lshlrev_b32_e32 v22, 16, v93
	v_and_b32_e32 v23, 0xffff0000, v93
	v_lshlrev_b32_e32 v24, 16, v94
	v_and_b32_e32 v25, 0xffff0000, v94
	v_lshlrev_b32_e32 v26, 16, v95
	v_and_b32_e32 v27, 0xffff0000, v95
	v_lshlrev_b32_e32 v28, 16, v96
	v_and_b32_e32 v29, 0xffff0000, v96
	v_lshlrev_b32_e32 v30, 16, v97
	v_and_b32_e32 v31, 0xffff0000, v97
	v_lshlrev_b32_e32 v32, 16, v98
	v_and_b32_e32 v33, 0xffff0000, v98
	v_lshlrev_b32_e32 v34, 16, v99
	v_and_b32_e32 v35, 0xffff0000, v99
	v_lshlrev_b32_e32 v36, 16, v100
	v_and_b32_e32 v37, 0xffff0000, v100
	v_lshlrev_b32_e32 v38, 16, v101
	v_and_b32_e32 v39, 0xffff0000, v101
	v_lshlrev_b32_e32 v40, 16, v102
	v_and_b32_e32 v41, 0xffff0000, v102
	v_lshlrev_b32_e32 v42, 16, v103
	v_and_b32_e32 v43, 0xffff0000, v103
	v_lshlrev_b32_e32 v44, 16, v104
	v_and_b32_e32 v45, 0xffff0000, v104
	v_lshlrev_b32_e32 v46, 16, v105
	v_and_b32_e32 v47, 0xffff0000, v105
	v_lshlrev_b32_e32 v48, 16, v106
	v_and_b32_e32 v49, 0xffff0000, v106
	v_lshlrev_b32_e32 v50, 16, v107
	v_and_b32_e32 v51, 0xffff0000, v107
	v_pk_mul_f32 v[232:233], v[20:21], v[20:21]
	v_pk_fma_f32 v[232:233], v[22:23], v[22:23], v[232:233]
	v_pk_fma_f32 v[232:233], v[24:25], v[24:25], v[232:233]
	v_pk_fma_f32 v[232:233], v[26:27], v[26:27], v[232:233]
	v_pk_fma_f32 v[232:233], v[28:29], v[28:29], v[232:233]
	v_pk_fma_f32 v[232:233], v[30:31], v[30:31], v[232:233]
	v_pk_fma_f32 v[232:233], v[32:33], v[32:33], v[232:233]
	v_pk_fma_f32 v[232:233], v[34:35], v[34:35], v[232:233]
	v_pk_fma_f32 v[232:233], v[36:37], v[36:37], v[232:233]
	v_pk_fma_f32 v[232:233], v[38:39], v[38:39], v[232:233]
	v_pk_fma_f32 v[232:233], v[40:41], v[40:41], v[232:233]
	v_pk_fma_f32 v[232:233], v[42:43], v[42:43], v[232:233]
	v_pk_fma_f32 v[232:233], v[44:45], v[44:45], v[232:233]
	v_pk_fma_f32 v[232:233], v[46:47], v[46:47], v[232:233]
	v_pk_fma_f32 v[232:233], v[48:49], v[48:49], v[232:233]
	v_pk_fma_f32 v[232:233], v[50:51], v[50:51], v[232:233]
	s_nop 0
	v_add_f32_e32 v232, v232, v233
	s_barrier
	ds_bpermute_b32 v233, v17, v232
	s_waitcnt lgkmcnt(0)
	v_add_f32_e32 v232, v232, v233
	v_mul_f32_e32 v232, 0x3c800000, v232
	v_add_f32_e32 v232, 0x358637bd, v232
	v_rsq_f32_e32 v232, v232
	s_nop 0
	v_mul_f32_e32 v20, v20, v232
	v_mul_f32_e32 v21, v21, v232
	v_mul_f32_e32 v22, v22, v232
	v_mul_f32_e32 v23, v23, v232
	v_mul_f32_e32 v24, v24, v232
	v_mul_f32_e32 v25, v25, v232
	v_mul_f32_e32 v26, v26, v232
	v_mul_f32_e32 v27, v27, v232
	v_mul_f32_e32 v28, v28, v232
	v_mul_f32_e32 v29, v29, v232
	v_mul_f32_e32 v30, v30, v232
	v_mul_f32_e32 v31, v31, v232
	v_mul_f32_e32 v32, v32, v232
	v_mul_f32_e32 v33, v33, v232
	v_mul_f32_e32 v34, v34, v232
	v_mul_f32_e32 v35, v35, v232
	v_mul_f32_e32 v36, v36, v232
	v_mul_f32_e32 v37, v37, v232
	v_mul_f32_e32 v38, v38, v232
	v_mul_f32_e32 v39, v39, v232
	v_mul_f32_e32 v40, v40, v232
	v_mul_f32_e32 v41, v41, v232
	v_mul_f32_e32 v42, v42, v232
	v_mul_f32_e32 v43, v43, v232
	v_mul_f32_e32 v44, v44, v232
	v_mul_f32_e32 v45, v45, v232
	v_mul_f32_e32 v46, v46, v232
	v_mul_f32_e32 v47, v47, v232
	v_mul_f32_e32 v48, v48, v232
	v_mul_f32_e32 v49, v49, v232
	v_mul_f32_e32 v50, v50, v232
	v_mul_f32_e32 v51, v51, v232
	v_mul_f32_e32 v20, v20, v148
	v_mul_f32_e32 v21, v21, v149
	v_mul_f32_e32 v22, v22, v150
	v_mul_f32_e32 v23, v23, v151
	v_mul_f32_e32 v24, v24, v152
	v_mul_f32_e32 v25, v25, v153
	v_mul_f32_e32 v26, v26, v154
	v_mul_f32_e32 v27, v27, v155
	v_mul_f32_e32 v28, v28, v156
	v_mul_f32_e32 v29, v29, v157
	v_mul_f32_e32 v30, v30, v158
	v_mul_f32_e32 v31, v31, v159
	v_mul_f32_e32 v32, v32, v160
	v_mul_f32_e32 v33, v33, v161
	v_mul_f32_e32 v34, v34, v162
	v_mul_f32_e32 v35, v35, v163
	v_mul_f32_e32 v36, v36, v164
	v_mul_f32_e32 v37, v37, v165
	v_mul_f32_e32 v38, v38, v166
	v_mul_f32_e32 v39, v39, v167
	v_mul_f32_e32 v40, v40, v168
	v_mul_f32_e32 v41, v41, v169
	v_mul_f32_e32 v42, v42, v170
	v_mul_f32_e32 v43, v43, v171
	v_mul_f32_e32 v44, v44, v172
	v_mul_f32_e32 v45, v45, v173
	v_mul_f32_e32 v46, v46, v174
	v_mul_f32_e32 v47, v47, v175
	v_mul_f32_e32 v48, v48, v176
	v_mul_f32_e32 v49, v49, v177
	v_mul_f32_e32 v50, v50, v178
	v_mul_f32_e32 v51, v51, v179
	v_cvt_pk_bf16_f32 v92, v20, v21
	v_cvt_pk_bf16_f32 v93, v22, v23
	v_cvt_pk_bf16_f32 v94, v24, v25
	v_cvt_pk_bf16_f32 v95, v26, v27
	v_cvt_pk_bf16_f32 v96, v28, v29
	v_cvt_pk_bf16_f32 v97, v30, v31
	v_cvt_pk_bf16_f32 v98, v32, v33
	v_cvt_pk_bf16_f32 v99, v34, v35
	v_cvt_pk_bf16_f32 v100, v36, v37
	v_cvt_pk_bf16_f32 v101, v38, v39
	v_cvt_pk_bf16_f32 v102, v40, v41
	v_cvt_pk_bf16_f32 v103, v42, v43
	v_cvt_pk_bf16_f32 v104, v44, v45
	v_cvt_pk_bf16_f32 v105, v46, v47
	v_cvt_pk_bf16_f32 v106, v48, v49
	v_cvt_pk_bf16_f32 v107, v50, v51
	ds_write_b128 v4, v[92:95] offset:0
	ds_write_b128 v4, v[96:99] offset:16
	ds_write_b128 v4, v[100:103] offset:32
	ds_write_b128 v4, v[104:107] offset:48
	s_bitcmp1_b32 s33, 0
	s_cbranch_scc1 .Lat_vodd
	ds_write2_b64 v5, v[112:113], v[114:115] offset0:0 offset1:1
	ds_write2_b64 v5, v[120:121], v[122:123] offset0:16 offset1:17
	ds_write2_b64 v5, v[128:129], v[130:131] offset0:32 offset1:33
	ds_write2_b64 v5, v[136:137], v[138:139] offset0:48 offset1:49
	s_branch .Lat_vwd
.Lat_vodd:
	ds_write2_b64 v5, v[112:113], v[114:115] offset0:1 offset1:0
	ds_write2_b64 v5, v[120:121], v[122:123] offset0:17 offset1:16
	ds_write2_b64 v5, v[128:129], v[130:131] offset0:33 offset1:32
	ds_write2_b64 v5, v[136:137], v[138:139] offset0:49 offset1:48
.Lat_vwd:
	s_lshl_b32 s4, s38, 2
	s_load_dword s54, s[26:27], s4
	s_waitcnt lgkmcnt(0)
	s_barrier
	s_add_i32 s39, s34, s91
	s_cmp_eq_u32 s38, s55
	s_cbranch_scc1 .Lat_bzdone
	s_mov_b32 s55, s38
	v_mov_b32_e32 v232, s54
	v_mul_f32_e32 v232, 0x3fb8aa3b, v232
	v_add_f32_e32 v232, 0xc1800000, v232
	v_exp_f32_e32 v88, v232
	s_lshl_b32 s2, s38, 9
	s_add_i32 s2, s2, 0x11400
	v_subrev_u32_e32 v233, 0, v18
	v_and_b32_e32 v233, 0x7f, v233
	v_lshl_add_u32 v233, v233, 2, s2
	ds_read_b32 v52, v233
	v_subrev_u32_e32 v233, 1, v18
	v_and_b32_e32 v233, 0x7f, v233
	v_lshl_add_u32 v233, v233, 2, s2
	ds_read_b32 v53, v233
	v_subrev_u32_e32 v233, 2, v18
	v_and_b32_e32 v233, 0x7f, v233
	v_lshl_add_u32 v233, v233, 2, s2
	ds_read_b32 v54, v233
	v_subrev_u32_e32 v233, 3, v18
	v_and_b32_e32 v233, 0x7f, v233
	v_lshl_add_u32 v233, v233, 2, s2
	ds_read_b32 v55, v233
	v_subrev_u32_e32 v233, 16, v18
	v_and_b32_e32 v233, 0x7f, v233
	v_lshl_add_u32 v233, v233, 2, s2
	ds_read_b32 v56, v233
	v_subrev_u32_e32 v233, 17, v18
	v_and_b32_e32 v233, 0x7f, v233
	v_lshl_add_u32 v233, v233, 2, s2
	ds_read_b32 v57, v233
	v_subrev_u32_e32 v233, 18, v18
	v_and_b32_e32 v233, 0x7f, v233
	v_lshl_add_u32 v233, v233, 2, s2
	ds_read_b32 v58, v233
	v_subrev_u32_e32 v233, 19, v18
	v_and_b32_e32 v233, 0x7f, v233
	v_lshl_add_u32 v233, v233, 2, s2
	ds_read_b32 v59, v233
	v_subrev_u32_e32 v233, 32, v18
	v_and_b32_e32 v233, 0x7f, v233
	v_lshl_add_u32 v233, v233, 2, s2
	ds_read_b32 v60, v233
	v_subrev_u32_e32 v233, 33, v18
	v_and_b32_e32 v233, 0x7f, v233
	v_lshl_add_u32 v233, v233, 2, s2
	ds_read_b32 v61, v233
	v_subrev_u32_e32 v233, 34, v18
	v_and_b32_e32 v233, 0x7f, v233
	v_lshl_add_u32 v233, v233, 2, s2
	ds_read_b32 v62, v233
	v_subrev_u32_e32 v233, 35, v18
	v_and_b32_e32 v233, 0x7f, v233
	v_lshl_add_u32 v233, v233, 2, s2
	ds_read_b32 v63, v233
	s_waitcnt lgkmcnt(0)
	v_subrev_u32_e32 v233, 48, v18
	v_and_b32_e32 v233, 0x7f, v233
	v_lshl_add_u32 v233, v233, 2, s2
	ds_read_b32 v64, v233
	v_subrev_u32_e32 v233, 49, v18
	v_and_b32_e32 v233, 0x7f, v233
	v_lshl_add_u32 v233, v233, 2, s2
	ds_read_b32 v65, v233
	v_subrev_u32_e32 v233, 50, v18
	v_and_b32_e32 v233, 0x7f, v233
	v_lshl_add_u32 v233, v233, 2, s2
	ds_read_b32 v66, v233
	v_subrev_u32_e32 v233, 51, v18
	v_and_b32_e32 v233, 0x7f, v233
	v_lshl_add_u32 v233, v233, 2, s2
	ds_read_b32 v67, v233
	v_subrev_u32_e32 v233, 64, v18
	v_and_b32_e32 v233, 0x7f, v233
	v_lshl_add_u32 v233, v233, 2, s2
	ds_read_b32 v68, v233
	v_subrev_u32_e32 v233, 0x41, v18
	v_and_b32_e32 v233, 0x7f, v233
	v_lshl_add_u32 v233, v233, 2, s2
	ds_read_b32 v69, v233
	v_subrev_u32_e32 v233, 0x42, v18
	v_and_b32_e32 v233, 0x7f, v233
	v_lshl_add_u32 v233, v233, 2, s2
	ds_read_b32 v70, v233
	v_subrev_u32_e32 v233, 0x43, v18
	v_and_b32_e32 v233, 0x7f, v233
	v_lshl_add_u32 v233, v233, 2, s2
	ds_read_b32 v71, v233
	v_subrev_u32_e32 v233, 0x50, v18
	v_and_b32_e32 v233, 0x7f, v233
	v_lshl_add_u32 v233, v233, 2, s2
	ds_read_b32 v72, v233
	v_subrev_u32_e32 v233, 0x51, v18
	v_and_b32_e32 v233, 0x7f, v233
	v_lshl_add_u32 v233, v233, 2, s2
	ds_read_b32 v73, v233
	v_subrev_u32_e32 v233, 0x52, v18
	v_and_b32_e32 v233, 0x7f, v233
	v_lshl_add_u32 v233, v233, 2, s2
	ds_read_b32 v74, v233
	v_subrev_u32_e32 v233, 0x53, v18
	v_and_b32_e32 v233, 0x7f, v233
	v_lshl_add_u32 v233, v233, 2, s2
	ds_read_b32 v75, v233
	s_waitcnt lgkmcnt(0)
	v_subrev_u32_e32 v233, 0x60, v18
	v_and_b32_e32 v233, 0x7f, v233
	v_lshl_add_u32 v233, v233, 2, s2
	ds_read_b32 v76, v233
	v_subrev_u32_e32 v233, 0x61, v18
	v_and_b32_e32 v233, 0x7f, v233
	v_lshl_add_u32 v233, v233, 2, s2
	ds_read_b32 v77, v233
	v_subrev_u32_e32 v233, 0x62, v18
	v_and_b32_e32 v233, 0x7f, v233
	v_lshl_add_u32 v233, v233, 2, s2
	ds_read_b32 v78, v233
	v_subrev_u32_e32 v233, 0x63, v18
	v_and_b32_e32 v233, 0x7f, v233
	v_lshl_add_u32 v233, v233, 2, s2
	ds_read_b32 v79, v233
	v_subrev_u32_e32 v233, 0x70, v18
	v_and_b32_e32 v233, 0x7f, v233
	v_lshl_add_u32 v233, v233, 2, s2
	ds_read_b32 v80, v233
	v_subrev_u32_e32 v233, 0x71, v18
	v_and_b32_e32 v233, 0x7f, v233
	v_lshl_add_u32 v233, v233, 2, s2
	ds_read_b32 v81, v233
	v_subrev_u32_e32 v233, 0x72, v18
	v_and_b32_e32 v233, 0x7f, v233
	v_lshl_add_u32 v233, v233, 2, s2
	ds_read_b32 v82, v233
	v_subrev_u32_e32 v233, 0x73, v18
	v_and_b32_e32 v233, 0x7f, v233
	v_lshl_add_u32 v233, v233, 2, s2
	ds_read_b32 v83, v233
	v_subrev_u32_e32 v233, 0x80, v18
	v_and_b32_e32 v233, 0x7f, v233
	v_lshl_add_u32 v233, v233, 2, s2
	ds_read_b32 v84, v233
	v_subrev_u32_e32 v233, 0x81, v18
	v_and_b32_e32 v233, 0x7f, v233
	v_lshl_add_u32 v233, v233, 2, s2
	ds_read_b32 v85, v233
	v_subrev_u32_e32 v233, 0x82, v18
	v_and_b32_e32 v233, 0x7f, v233
	v_lshl_add_u32 v233, v233, 2, s2
	ds_read_b32 v86, v233
	v_subrev_u32_e32 v233, 0x83, v18
	v_and_b32_e32 v233, 0x7f, v233
	v_lshl_add_u32 v233, v233, 2, s2
	ds_read_b32 v87, v233
	s_waitcnt lgkmcnt(0)
	s_waitcnt lgkmcnt(0)
	v_mov_b32_e32 v235, 0x80
	v_subrev_u32_e32 v233, 0, v18
	v_subrev_u32_e32 v234, 1, v18
	v_cmp_gt_u32_e32 vcc, 0x80, v233
	v_cmp_lt_u32_e64 s[6:7], v234, v235
	s_nop 0
	v_cndmask_b32_e32 v52, v89, v52, vcc
	v_cndmask_b32_e64 v53, v89, v53, s[6:7]
	v_subrev_u32_e32 v233, 2, v18
	v_subrev_u32_e32 v234, 3, v18
	v_cmp_gt_u32_e32 vcc, 0x80, v233
	v_cmp_lt_u32_e64 s[6:7], v234, v235
	s_nop 0
	v_cndmask_b32_e32 v54, v89, v54, vcc
	v_cndmask_b32_e64 v55, v89, v55, s[6:7]
	v_subrev_u32_e32 v233, 16, v18
	v_subrev_u32_e32 v234, 17, v18
	v_cmp_gt_u32_e32 vcc, 0x80, v233
	v_cmp_lt_u32_e64 s[6:7], v234, v235
	s_nop 0
	v_cndmask_b32_e32 v56, v89, v56, vcc
	v_cndmask_b32_e64 v57, v89, v57, s[6:7]
	v_subrev_u32_e32 v233, 18, v18
	v_subrev_u32_e32 v234, 19, v18
	v_cmp_gt_u32_e32 vcc, 0x80, v233
	v_cmp_lt_u32_e64 s[6:7], v234, v235
	s_nop 0
	v_cndmask_b32_e32 v58, v89, v58, vcc
	v_cndmask_b32_e64 v59, v89, v59, s[6:7]
	v_subrev_u32_e32 v233, 32, v18
	v_subrev_u32_e32 v234, 33, v18
	v_cmp_gt_u32_e32 vcc, 0x80, v233
	v_cmp_lt_u32_e64 s[6:7], v234, v235
	s_nop 0
	v_cndmask_b32_e32 v60, v89, v60, vcc
	v_cndmask_b32_e64 v61, v89, v61, s[6:7]
	v_subrev_u32_e32 v233, 34, v18
	v_subrev_u32_e32 v234, 35, v18
	v_cmp_gt_u32_e32 vcc, 0x80, v233
	v_cmp_lt_u32_e64 s[6:7], v234, v235
	s_nop 0
	v_cndmask_b32_e32 v62, v89, v62, vcc
	v_cndmask_b32_e64 v63, v89, v63, s[6:7]
	v_subrev_u32_e32 v233, 48, v18
	v_subrev_u32_e32 v234, 49, v18
	v_cmp_gt_u32_e32 vcc, 0x80, v233
	v_cmp_lt_u32_e64 s[6:7], v234, v235
	s_nop 0
	v_cndmask_b32_e32 v64, v89, v64, vcc
	v_cndmask_b32_e64 v65, v89, v65, s[6:7]
	v_subrev_u32_e32 v233, 50, v18
	v_subrev_u32_e32 v234, 51, v18
	v_cmp_gt_u32_e32 vcc, 0x80, v233
	v_cmp_lt_u32_e64 s[6:7], v234, v235
	s_nop 0
	v_cndmask_b32_e32 v66, v89, v66, vcc
	v_cndmask_b32_e64 v67, v89, v67, s[6:7]
	v_subrev_u32_e32 v233, 64, v18
	v_subrev_u32_e32 v234, 0x41, v18
	v_cmp_gt_u32_e32 vcc, 0x80, v233
	v_cmp_lt_u32_e64 s[6:7], v234, v235
	s_nop 0
	v_cndmask_b32_e32 v68, v89, v68, vcc
	v_cndmask_b32_e64 v69, v89, v69, s[6:7]
	v_subrev_u32_e32 v233, 0x42, v18
	v_subrev_u32_e32 v234, 0x43, v18
	v_cmp_gt_u32_e32 vcc, 0x80, v233
	v_cmp_lt_u32_e64 s[6:7], v234, v235
	s_nop 0
	v_cndmask_b32_e32 v70, v89, v70, vcc
	v_cndmask_b32_e64 v71, v89, v71, s[6:7]
	v_subrev_u32_e32 v233, 0x50, v18
	v_subrev_u32_e32 v234, 0x51, v18
	v_cmp_gt_u32_e32 vcc, 0x80, v233
	v_cmp_lt_u32_e64 s[6:7], v234, v235
	s_nop 0
	v_cndmask_b32_e32 v72, v89, v72, vcc
	v_cndmask_b32_e64 v73, v89, v73, s[6:7]
	v_subrev_u32_e32 v233, 0x52, v18
	v_subrev_u32_e32 v234, 0x53, v18
	v_cmp_gt_u32_e32 vcc, 0x80, v233
	v_cmp_lt_u32_e64 s[6:7], v234, v235
	s_nop 0
	v_cndmask_b32_e32 v74, v89, v74, vcc
	v_cndmask_b32_e64 v75, v89, v75, s[6:7]
	v_subrev_u32_e32 v233, 0x60, v18
	v_subrev_u32_e32 v234, 0x61, v18
	v_cmp_gt_u32_e32 vcc, 0x80, v233
	v_cmp_lt_u32_e64 s[6:7], v234, v235
	s_nop 0
	v_cndmask_b32_e32 v76, v89, v76, vcc
	v_cndmask_b32_e64 v77, v89, v77, s[6:7]
	v_subrev_u32_e32 v233, 0x62, v18
	v_subrev_u32_e32 v234, 0x63, v18
	v_cmp_gt_u32_e32 vcc, 0x80, v233
	v_cmp_lt_u32_e64 s[6:7], v234, v235
	s_nop 0
	v_cndmask_b32_e32 v78, v89, v78, vcc
	v_cndmask_b32_e64 v79, v89, v79, s[6:7]
	v_subrev_u32_e32 v233, 0x70, v18
	v_subrev_u32_e32 v234, 0x71, v18
	v_cmp_gt_u32_e32 vcc, 0x80, v233
	v_cmp_lt_u32_e64 s[6:7], v234, v235
	s_nop 0
	v_cndmask_b32_e32 v80, v89, v80, vcc
	v_cndmask_b32_e64 v81, v89, v81, s[6:7]
	v_subrev_u32_e32 v233, 0x72, v18
	v_subrev_u32_e32 v234, 0x73, v18
	v_cmp_gt_u32_e32 vcc, 0x80, v233
	v_cmp_lt_u32_e64 s[6:7], v234, v235
	s_nop 0
	v_cndmask_b32_e32 v82, v89, v82, vcc
	v_cndmask_b32_e64 v83, v89, v83, s[6:7]
	v_subrev_u32_e32 v233, 0x80, v18
	v_subrev_u32_e32 v234, 0x81, v18
	v_cmp_gt_u32_e32 vcc, 0x80, v233
	v_cmp_lt_u32_e64 s[6:7], v234, v235
	s_nop 0
	v_cndmask_b32_e32 v84, v89, v84, vcc
	v_cndmask_b32_e64 v85, v89, v85, s[6:7]
	v_subrev_u32_e32 v233, 0x82, v18
	v_subrev_u32_e32 v234, 0x83, v18
	v_cmp_gt_u32_e32 vcc, 0x80, v233
	v_cmp_lt_u32_e64 s[6:7], v234, v235
	s_nop 0
	v_cndmask_b32_e32 v86, v89, v86, vcc
	v_cndmask_b32_e64 v87, v89, v87, s[6:7]
.Lat_bzdone:
	ds_read_b128 v[20:23], v10 offset:0
	ds_read_b128 v[24:27], v10 offset:64
	ds_read_b128 v[28:31], v10 offset:2304
	ds_read_b128 v[32:35], v10 offset:2368
	ds_read_b128 v[36:39], v10 offset:4608
	ds_read_b128 v[40:43], v10 offset:4672
	ds_read_b128 v[44:47], v10 offset:6912
	ds_read_b128 v[48:51], v10 offset:6976
	ds_read_b128 v[216:219], v10 offset:9216
	ds_read_b128 v[220:223], v10 offset:9280
	s_waitcnt vmcnt(0)
	v_lshlrev_b32_e32 v234, 16, v184
	v_and_b32_e32 v235, 0xffff0000, v184
	v_pk_mul_f32 v[232:233], v[234:235], v[234:235]
	v_lshlrev_b32_e32 v228, 16, v192
	v_and_b32_e32 v229, 0xffff0000, v192
	v_pk_mul_f32 v[226:227], v[228:229], v[228:229]
	v_lshlrev_b32_e32 v234, 16, v185
	v_and_b32_e32 v235, 0xffff0000, v185
	v_pk_fma_f32 v[232:233], v[234:235], v[234:235], v[232:233]
	v_lshlrev_b32_e32 v228, 16, v193
	v_and_b32_e32 v229, 0xffff0000, v193
	v_pk_fma_f32 v[226:227], v[228:229], v[228:229], v[226:227]
	v_lshlrev_b32_e32 v234, 16, v186
	v_and_b32_e32 v235, 0xffff0000, v186
	v_pk_fma_f32 v[232:233], v[234:235], v[234:235], v[232:233]
	v_lshlrev_b32_e32 v228, 16, v194
	v_and_b32_e32 v229, 0xffff0000, v194
	v_pk_fma_f32 v[226:227], v[228:229], v[228:229], v[226:227]
	v_lshlrev_b32_e32 v234, 16, v187
	v_and_b32_e32 v235, 0xffff0000, v187
	v_pk_fma_f32 v[232:233], v[234:235], v[234:235], v[232:233]
	v_lshlrev_b32_e32 v228, 16, v195
	v_and_b32_e32 v229, 0xffff0000, v195
	v_pk_fma_f32 v[226:227], v[228:229], v[228:229], v[226:227]
	v_lshlrev_b32_e32 v234, 16, v188
	v_and_b32_e32 v235, 0xffff0000, v188
	v_pk_fma_f32 v[232:233], v[234:235], v[234:235], v[232:233]
	v_lshlrev_b32_e32 v228, 16, v196
	v_and_b32_e32 v229, 0xffff0000, v196
	v_pk_fma_f32 v[226:227], v[228:229], v[228:229], v[226:227]
	v_lshlrev_b32_e32 v234, 16, v189
	v_and_b32_e32 v235, 0xffff0000, v189
	v_pk_fma_f32 v[232:233], v[234:235], v[234:235], v[232:233]
	v_lshlrev_b32_e32 v228, 16, v197
	v_and_b32_e32 v229, 0xffff0000, v197
	v_pk_fma_f32 v[226:227], v[228:229], v[228:229], v[226:227]
	v_lshlrev_b32_e32 v234, 16, v190
	v_and_b32_e32 v235, 0xffff0000, v190
	v_pk_fma_f32 v[232:233], v[234:235], v[234:235], v[232:233]
	v_lshlrev_b32_e32 v228, 16, v198
	v_and_b32_e32 v229, 0xffff0000, v198
	v_pk_fma_f32 v[226:227], v[228:229], v[228:229], v[226:227]
	v_lshlrev_b32_e32 v234, 16, v191
	v_and_b32_e32 v235, 0xffff0000, v191
	v_pk_fma_f32 v[232:233], v[234:235], v[234:235], v[232:233]
	v_lshlrev_b32_e32 v228, 16, v199
	v_and_b32_e32 v229, 0xffff0000, v199
	v_pk_fma_f32 v[226:227], v[228:229], v[228:229], v[226:227]
	v_add_f32_e32 v232, v232, v233
	v_add_f32_e32 v226, v226, v227
	s_nop 0
	ds_bpermute_b32 v233, v15, v232
	ds_bpermute_b32 v227, v15, v226
	s_waitcnt lgkmcnt(6)
	v_mfma_f32_16x16x32_bf16 v[108:111], v[20:23], v[184:187], 0
	v_mfma_f32_16x16x32_bf16 v[112:115], v[28:31], v[184:187], 0
	v_mfma_f32_16x16x32_bf16 v[148:151], v[28:31], v[192:195], 0
	v_mfma_f32_16x16x32_bf16 v[116:119], v[36:39], v[184:187], 0
	v_mfma_f32_16x16x32_bf16 v[152:155], v[36:39], v[192:195], 0
	v_mfma_f32_16x16x32_bf16 v[108:111], v[24:27], v[188:191], v[108:111]
	v_mfma_f32_16x16x32_bf16 v[112:115], v[32:35], v[188:191], v[112:115]
	v_mfma_f32_16x16x32_bf16 v[148:151], v[32:35], v[196:199], v[148:151]
	v_mfma_f32_16x16x32_bf16 v[116:119], v[40:43], v[188:191], v[116:119]
	v_mfma_f32_16x16x32_bf16 v[152:155], v[40:43], v[196:199], v[152:155]
	ds_read_b128 v[20:23], v10 offset:11520
	ds_read_b128 v[24:27], v10 offset:11584
	ds_read_b128 v[28:31], v10 offset:13824
	ds_read_b128 v[32:35], v10 offset:13888
	ds_read_b128 v[36:39], v10 offset:16128
	ds_read_b128 v[40:43], v10 offset:16192
	s_waitcnt lgkmcnt(6)
	v_add_f32_e32 v232, v232, v233
	v_add_f32_e32 v226, v226, v227
	s_nop 0
	ds_bpermute_b32 v233, v16, v232
	ds_bpermute_b32 v227, v16, v226
	v_mfma_f32_16x16x32_bf16 v[120:123], v[44:47], v[184:187], 0
	v_mfma_f32_16x16x32_bf16 v[156:159], v[44:47], v[192:195], 0
	v_mfma_f32_16x16x32_bf16 v[124:127], v[216:219], v[184:187], 0
	v_mfma_f32_16x16x32_bf16 v[160:163], v[216:219], v[192:195], 0
	v_mfma_f32_16x16x32_bf16 v[120:123], v[48:51], v[188:191], v[120:123]
	v_mfma_f32_16x16x32_bf16 v[156:159], v[48:51], v[196:199], v[156:159]
	v_mfma_f32_16x16x32_bf16 v[124:127], v[220:223], v[188:191], v[124:127]
	v_mfma_f32_16x16x32_bf16 v[160:163], v[220:223], v[196:199], v[160:163]
	ds_read_b128 v[44:47], v10 offset:18432
	ds_read_b128 v[48:51], v10 offset:18496
	ds_read_b128 v[216:219], v10 offset:20736
	ds_read_b128 v[220:223], v10 offset:20800
	s_waitcnt lgkmcnt(6)
	v_mfma_f32_16x16x32_bf16 v[128:131], v[20:23], v[184:187], 0
	v_mfma_f32_16x16x32_bf16 v[164:167], v[20:23], v[192:195], 0
	v_mfma_f32_16x16x32_bf16 v[132:135], v[28:31], v[184:187], 0
	v_mfma_f32_16x16x32_bf16 v[168:171], v[28:31], v[192:195], 0
	v_mfma_f32_16x16x32_bf16 v[136:139], v[36:39], v[184:187], 0
	v_mfma_f32_16x16x32_bf16 v[172:175], v[36:39], v[192:195], 0
	v_mfma_f32_16x16x32_bf16 v[128:131], v[24:27], v[188:191], v[128:131]
	v_mfma_f32_16x16x32_bf16 v[164:167], v[24:27], v[196:199], v[164:167]
	v_mfma_f32_16x16x32_bf16 v[132:135], v[32:35], v[188:191], v[132:135]
	v_mfma_f32_16x16x32_bf16 v[168:171], v[32:35], v[196:199], v[168:171]
	v_mfma_f32_16x16x32_bf16 v[136:139], v[40:43], v[188:191], v[136:139]
	v_mfma_f32_16x16x32_bf16 v[172:175], v[40:43], v[196:199], v[172:175]
	s_waitcnt lgkmcnt(0)
	v_mfma_f32_16x16x32_bf16 v[140:143], v[44:47], v[184:187], 0
	v_mfma_f32_16x16x32_bf16 v[176:179], v[44:47], v[192:195], 0
	v_mfma_f32_16x16x32_bf16 v[180:183], v[216:219], v[192:195], 0
	v_mfma_f32_16x16x32_bf16 v[140:143], v[48:51], v[188:191], v[140:143]
	v_mfma_f32_16x16x32_bf16 v[176:179], v[48:51], v[196:199], v[176:179]
	v_mfma_f32_16x16x32_bf16 v[180:183], v[220:223], v[196:199], v[180:183]
	s_add_u32 s48, s48, 0x28000
	s_addc_u32 s49, s49, 0
	s_add_u32 s58, s58, 0x28000
	s_addc_u32 s59, s59, 0
	global_load_dwordx4 v[92:95], v8, s[48:49]
	global_load_dwordx4 v[96:99], v8, s[48:49] offset:64
	global_load_dwordx4 v[100:103], v8, s[58:59]
	global_load_dwordx4 v[104:107], v8, s[58:59] offset:64
	ds_read2_b64 v[20:23], v11 offset0:0 offset1:4
	ds_read2_b64 v[24:27], v12 offset0:0 offset1:4
	ds_read2_b64 v[28:31], v13 offset0:0 offset1:4
	ds_read2_b64 v[32:35], v14 offset0:0 offset1:4
	ds_read2_b64 v[36:39], v11 offset0:8 offset1:12
	ds_read2_b64 v[40:43], v12 offset0:8 offset1:12
	ds_read2_b64 v[44:47], v13 offset0:8 offset1:12
	ds_read2_b64 v[48:51], v14 offset0:8 offset1:12
	v_add_f32_e32 v232, v232, v233
	v_add_f32_e32 v226, v226, v227
	v_mul_f32_e32 v232, 0x3c800000, v232
	v_mul_f32_e32 v226, 0x3c800000, v226
	v_add_f32_e32 v232, 0x358637bd, v232
	v_add_f32_e32 v226, 0x358637bd, v226
	v_rsq_f32_e32 v236, v232
	v_rsq_f32_e32 v230, v226
	v_mov_b32_e32 v237, v236
	v_mov_b32_e32 v231, v230
	s_nop 1
	v_pk_fma_f32 v[108:109], v[108:109], v[236:237], v[52:53]
	v_pk_fma_f32 v[110:111], v[110:111], v[236:237], v[54:55]
	v_pk_fma_f32 v[148:149], v[148:149], v[230:231], v[52:53]
	v_pk_fma_f32 v[150:151], v[150:151], v[230:231], v[54:55]
	v_pk_fma_f32 v[112:113], v[112:113], v[236:237], v[56:57]
	v_pk_fma_f32 v[114:115], v[114:115], v[236:237], v[58:59]
	v_pk_fma_f32 v[152:153], v[152:153], v[230:231], v[56:57]
	v_pk_fma_f32 v[154:155], v[154:155], v[230:231], v[58:59]
	v_pk_fma_f32 v[116:117], v[116:117], v[236:237], v[60:61]
	v_pk_fma_f32 v[118:119], v[118:119], v[236:237], v[62:63]
	v_pk_fma_f32 v[156:157], v[156:157], v[230:231], v[60:61]
	v_pk_fma_f32 v[158:159], v[158:159], v[230:231], v[62:63]
	v_pk_fma_f32 v[120:121], v[120:121], v[236:237], v[64:65]
	v_pk_fma_f32 v[122:123], v[122:123], v[236:237], v[66:67]
	v_pk_fma_f32 v[160:161], v[160:161], v[230:231], v[64:65]
	v_pk_fma_f32 v[162:163], v[162:163], v[230:231], v[66:67]
	v_pk_fma_f32 v[124:125], v[124:125], v[236:237], v[68:69]
	v_pk_fma_f32 v[126:127], v[126:127], v[236:237], v[70:71]
	v_pk_fma_f32 v[164:165], v[164:165], v[230:231], v[68:69]
	v_pk_fma_f32 v[166:167], v[166:167], v[230:231], v[70:71]
	v_pk_fma_f32 v[128:129], v[128:129], v[236:237], v[72:73]
	v_pk_fma_f32 v[130:131], v[130:131], v[236:237], v[74:75]
	v_pk_fma_f32 v[168:169], v[168:169], v[230:231], v[72:73]
	v_pk_fma_f32 v[170:171], v[170:171], v[230:231], v[74:75]
	v_pk_fma_f32 v[132:133], v[132:133], v[236:237], v[76:77]
	v_pk_fma_f32 v[134:135], v[134:135], v[236:237], v[78:79]
	v_pk_fma_f32 v[172:173], v[172:173], v[230:231], v[76:77]
	v_pk_fma_f32 v[174:175], v[174:175], v[230:231], v[78:79]
	v_pk_fma_f32 v[136:137], v[136:137], v[236:237], v[80:81]
	v_pk_fma_f32 v[138:139], v[138:139], v[236:237], v[82:83]
	v_pk_fma_f32 v[176:177], v[176:177], v[230:231], v[80:81]
	v_pk_fma_f32 v[178:179], v[178:179], v[230:231], v[82:83]
	v_pk_fma_f32 v[140:141], v[140:141], v[236:237], v[84:85]
	v_pk_fma_f32 v[142:143], v[142:143], v[236:237], v[86:87]
	v_pk_fma_f32 v[180:181], v[180:181], v[230:231], v[84:85]
	v_pk_fma_f32 v[182:183], v[182:183], v[230:231], v[86:87]
	v_exp_f32_e32 v108, v108
	v_exp_f32_e32 v109, v109
	v_exp_f32_e32 v110, v110
	v_exp_f32_e32 v111, v111
	v_exp_f32_e32 v148, v148
	v_exp_f32_e32 v149, v149
	v_exp_f32_e32 v150, v150
	v_exp_f32_e32 v151, v151
	v_exp_f32_e32 v112, v112
	v_exp_f32_e32 v113, v113
	v_exp_f32_e32 v114, v114
	v_exp_f32_e32 v115, v115
	v_exp_f32_e32 v152, v152
	v_exp_f32_e32 v153, v153
	v_exp_f32_e32 v154, v154
	v_exp_f32_e32 v155, v155
	v_exp_f32_e32 v116, v116
	v_exp_f32_e32 v117, v117
	v_exp_f32_e32 v118, v118
	v_exp_f32_e32 v119, v119
	v_exp_f32_e32 v156, v156
	v_exp_f32_e32 v157, v157
	v_exp_f32_e32 v158, v158
	v_exp_f32_e32 v159, v159
	v_exp_f32_e32 v120, v120
	v_exp_f32_e32 v121, v121
	v_exp_f32_e32 v122, v122
	v_exp_f32_e32 v123, v123
	v_exp_f32_e32 v160, v160
	v_exp_f32_e32 v161, v161
	v_exp_f32_e32 v162, v162
	v_exp_f32_e32 v163, v163
	v_exp_f32_e32 v124, v124
	v_exp_f32_e32 v125, v125
	v_exp_f32_e32 v126, v126
	v_exp_f32_e32 v127, v127
	v_exp_f32_e32 v164, v164
	v_exp_f32_e32 v165, v165
	v_exp_f32_e32 v166, v166
	v_exp_f32_e32 v167, v167
	v_exp_f32_e32 v128, v128
	v_exp_f32_e32 v129, v129
	v_exp_f32_e32 v130, v130
	v_exp_f32_e32 v131, v131
	v_exp_f32_e32 v168, v168
	v_exp_f32_e32 v169, v169
	v_exp_f32_e32 v170, v170
	v_exp_f32_e32 v171, v171
	v_exp_f32_e32 v132, v132
	v_exp_f32_e32 v133, v133
	v_exp_f32_e32 v134, v134
	v_exp_f32_e32 v135, v135
	v_exp_f32_e32 v172, v172
	v_exp_f32_e32 v173, v173
	v_exp_f32_e32 v174, v174
	v_exp_f32_e32 v175, v175
	v_exp_f32_e32 v136, v136
	v_exp_f32_e32 v137, v137
	v_exp_f32_e32 v138, v138
	v_exp_f32_e32 v139, v139
	v_exp_f32_e32 v176, v176
	v_exp_f32_e32 v177, v177
	v_exp_f32_e32 v178, v178
	v_exp_f32_e32 v179, v179
	v_exp_f32_e32 v140, v140
	v_exp_f32_e32 v141, v141
	v_exp_f32_e32 v142, v142
	v_exp_f32_e32 v143, v143
	v_exp_f32_e32 v180, v180
	v_exp_f32_e32 v181, v181
	v_exp_f32_e32 v182, v182
	v_exp_f32_e32 v183, v183
	s_cmp_lg_u32 s36, 0
	s_cbranch_scc1 .Lat_m0
	v_mov_b32_e32 v108, 0
	v_mov_b32_e32 v109, 0
	v_mov_b32_e32 v110, 0
	v_mov_b32_e32 v111, 0
	v_mov_b32_e32 v112, 0
	v_mov_b32_e32 v113, 0
	v_mov_b32_e32 v114, 0
	v_mov_b32_e32 v115, 0
	v_mov_b32_e32 v116, 0
	v_mov_b32_e32 v117, 0
	v_mov_b32_e32 v118, 0
	v_mov_b32_e32 v119, 0
	v_mov_b32_e32 v120, 0
	v_mov_b32_e32 v121, 0
	v_mov_b32_e32 v122, 0
	v_mov_b32_e32 v123, 0
	v_mov_b32_e32 v124, 0
	v_mov_b32_e32 v125, 0
	v_mov_b32_e32 v126, 0
	v_mov_b32_e32 v127, 0
	v_mov_b32_e32 v128, 0
	v_mov_b32_e32 v129, 0
	v_mov_b32_e32 v130, 0
	v_mov_b32_e32 v131, 0
	v_mov_b32_e32 v132, 0
	v_mov_b32_e32 v133, 0
	v_mov_b32_e32 v134, 0
	v_mov_b32_e32 v135, 0
	v_mov_b32_e32 v136, 0
	v_mov_b32_e32 v137, 0
	v_mov_b32_e32 v138, 0
	v_mov_b32_e32 v139, 0
	v_mov_b32_e32 v148, 0
	v_mov_b32_e32 v149, 0
	v_mov_b32_e32 v150, 0
	v_mov_b32_e32 v151, 0
	v_mov_b32_e32 v152, 0
	v_mov_b32_e32 v153, 0
	v_mov_b32_e32 v154, 0
	v_mov_b32_e32 v155, 0
	v_mov_b32_e32 v156, 0
	v_mov_b32_e32 v157, 0
	v_mov_b32_e32 v158, 0
	v_mov_b32_e32 v159, 0
	v_mov_b32_e32 v160, 0
	v_mov_b32_e32 v161, 0
	v_mov_b32_e32 v162, 0
	v_mov_b32_e32 v163, 0
	v_mov_b32_e32 v164, 0
	v_mov_b32_e32 v165, 0
	v_mov_b32_e32 v166, 0
	v_mov_b32_e32 v167, 0
	v_mov_b32_e32 v168, 0
	v_mov_b32_e32 v169, 0
	v_mov_b32_e32 v170, 0
	v_mov_b32_e32 v171, 0
	v_mov_b32_e32 v172, 0
	v_mov_b32_e32 v173, 0
	v_mov_b32_e32 v174, 0
	v_mov_b32_e32 v175, 0
.Lat_m0:
	s_nop 0
	v_pk_add_f32 v[232:233], v[108:109], v[110:111]
	v_pk_add_f32 v[234:235], v[112:113], v[114:115]
	v_pk_add_f32 v[226:227], v[148:149], v[150:151]
	v_pk_add_f32 v[228:229], v[152:153], v[154:155]
	v_pk_add_f32 v[232:233], v[232:233], v[116:117]
	v_pk_add_f32 v[234:235], v[234:235], v[118:119]
	v_pk_add_f32 v[226:227], v[226:227], v[156:157]
	v_pk_add_f32 v[228:229], v[228:229], v[158:159]
	v_pk_add_f32 v[232:233], v[232:233], v[120:121]
	v_pk_add_f32 v[234:235], v[234:235], v[122:123]
	v_pk_add_f32 v[226:227], v[226:227], v[160:161]
	v_pk_add_f32 v[228:229], v[228:229], v[162:163]
	v_pk_add_f32 v[232:233], v[232:233], v[124:125]
	v_pk_add_f32 v[234:235], v[234:235], v[126:127]
	v_pk_add_f32 v[226:227], v[226:227], v[164:165]
	v_pk_add_f32 v[228:229], v[228:229], v[166:167]
	v_pk_add_f32 v[232:233], v[232:233], v[128:129]
	v_pk_add_f32 v[234:235], v[234:235], v[130:131]
	v_pk_add_f32 v[226:227], v[226:227], v[168:169]
	v_pk_add_f32 v[228:229], v[228:229], v[170:171]
	v_pk_add_f32 v[232:233], v[232:233], v[132:133]
	v_pk_add_f32 v[234:235], v[234:235], v[134:135]
	v_pk_add_f32 v[226:227], v[226:227], v[172:173]
	v_pk_add_f32 v[228:229], v[228:229], v[174:175]
	v_pk_add_f32 v[232:233], v[232:233], v[136:137]
	v_pk_add_f32 v[234:235], v[234:235], v[138:139]
	v_pk_add_f32 v[226:227], v[226:227], v[176:177]
	v_pk_add_f32 v[228:229], v[228:229], v[178:179]
	v_pk_add_f32 v[232:233], v[232:233], v[140:141]
	v_pk_add_f32 v[234:235], v[234:235], v[142:143]
	v_pk_add_f32 v[226:227], v[226:227], v[180:181]
	v_pk_add_f32 v[228:229], v[228:229], v[182:183]
	v_pk_add_f32 v[232:233], v[232:233], v[234:235]
	v_pk_add_f32 v[226:227], v[226:227], v[228:229]
	v_add_f32_e32 v232, v232, v233
	v_add_f32_e32 v226, v226, v227
	v_cvt_pk_bf16_f32 v108, v108, v109
	v_cvt_pk_bf16_f32 v109, v110, v111
	v_cvt_pk_bf16_f32 v110, v112, v113
	v_cvt_pk_bf16_f32 v111, v114, v115
	v_cvt_pk_bf16_f32 v146, v148, v149
	v_cvt_pk_bf16_f32 v147, v150, v151
	v_cvt_pk_bf16_f32 v116, v116, v117
	v_cvt_pk_bf16_f32 v117, v118, v119
	v_cvt_pk_bf16_f32 v118, v120, v121
	v_cvt_pk_bf16_f32 v119, v122, v123
	v_cvt_pk_bf16_f32 v152, v152, v153
	v_cvt_pk_bf16_f32 v153, v154, v155
	v_cvt_pk_bf16_f32 v154, v156, v157
	v_cvt_pk_bf16_f32 v155, v158, v159
	v_cvt_pk_bf16_f32 v124, v124, v125
	v_cvt_pk_bf16_f32 v125, v126, v127
	v_cvt_pk_bf16_f32 v126, v128, v129
	v_cvt_pk_bf16_f32 v127, v130, v131
	v_cvt_pk_bf16_f32 v160, v160, v161
	v_cvt_pk_bf16_f32 v161, v162, v163
	v_cvt_pk_bf16_f32 v162, v164, v165
	v_cvt_pk_bf16_f32 v163, v166, v167
	v_cvt_pk_bf16_f32 v132, v132, v133
	v_cvt_pk_bf16_f32 v133, v134, v135
	v_cvt_pk_bf16_f32 v134, v136, v137
	v_cvt_pk_bf16_f32 v135, v138, v139
	v_cvt_pk_bf16_f32 v168, v168, v169
	v_cvt_pk_bf16_f32 v169, v170, v171
	v_cvt_pk_bf16_f32 v170, v172, v173
	v_cvt_pk_bf16_f32 v171, v174, v175
	v_cvt_pk_bf16_f32 v140, v140, v141
	v_cvt_pk_bf16_f32 v141, v142, v143
	v_mov_b32_e32 v142, 0
	v_mov_b32_e32 v143, 0
	v_cvt_pk_bf16_f32 v176, v176, v177
	v_cvt_pk_bf16_f32 v177, v178, v179
	v_cvt_pk_bf16_f32 v178, v180, v181
	v_cvt_pk_bf16_f32 v179, v182, v183
	ds_bpermute_b32 v233, v15, v232
	ds_bpermute_b32 v227, v15, v226
	s_waitcnt lgkmcnt(2)
	v_mfma_f32_16x16x32_bf16 v[184:187], v[20:23], v[108:111], 0
	v_mfma_f32_16x16x32_bf16 v[188:191], v[24:27], v[108:111], 0
	v_mfma_f32_16x16x32_bf16 v[192:195], v[28:31], v[108:111], 0
	v_mfma_f32_16x16x32_bf16 v[196:199], v[32:35], v[108:111], 0
	v_mfma_f32_16x16x32_bf16 v[200:203], v[20:23], v[144:147], 0
	v_mfma_f32_16x16x32_bf16 v[204:207], v[24:27], v[144:147], 0
	v_mfma_f32_16x16x32_bf16 v[208:211], v[28:31], v[144:147], 0
	v_mfma_f32_16x16x32_bf16 v[212:215], v[32:35], v[144:147], 0
	ds_read2_b64 v[20:23], v11 offset0:16 offset1:20
	ds_read2_b64 v[24:27], v12 offset0:16 offset1:20
	ds_read2_b64 v[28:31], v13 offset0:16 offset1:20
	ds_read2_b64 v[32:35], v14 offset0:16 offset1:20
	v_mfma_f32_16x16x32_bf16 v[184:187], v[36:39], v[116:119], v[184:187]
	v_mfma_f32_16x16x32_bf16 v[188:191], v[40:43], v[116:119], v[188:191]
	v_mfma_f32_16x16x32_bf16 v[192:195], v[44:47], v[116:119], v[192:195]
	v_mfma_f32_16x16x32_bf16 v[196:199], v[48:51], v[116:119], v[196:199]
	v_mfma_f32_16x16x32_bf16 v[200:203], v[36:39], v[152:155], v[200:203]
	v_mfma_f32_16x16x32_bf16 v[204:207], v[40:43], v[152:155], v[204:207]
	v_mfma_f32_16x16x32_bf16 v[208:211], v[44:47], v[152:155], v[208:211]
	v_mfma_f32_16x16x32_bf16 v[212:215], v[48:51], v[152:155], v[212:215]
	ds_read2_b64 v[36:39], v11 offset0:24 offset1:28
	ds_read2_b64 v[40:43], v12 offset0:24 offset1:28
	ds_read2_b64 v[44:47], v13 offset0:24 offset1:28
	ds_read2_b64 v[48:51], v14 offset0:24 offset1:28
	s_waitcnt lgkmcnt(8)
	v_add_f32_e32 v232, v232, v233
	v_add_f32_e32 v226, v226, v227
	s_nop 0
	ds_bpermute_b32 v233, v16, v232
	ds_bpermute_b32 v227, v16, v226
	s_waitcnt lgkmcnt(6)
	v_mfma_f32_16x16x32_bf16 v[184:187], v[20:23], v[124:127], v[184:187]
	v_mfma_f32_16x16x32_bf16 v[188:191], v[24:27], v[124:127], v[188:191]
	v_mfma_f32_16x16x32_bf16 v[192:195], v[28:31], v[124:127], v[192:195]
	v_mfma_f32_16x16x32_bf16 v[196:199], v[32:35], v[124:127], v[196:199]
	v_mfma_f32_16x16x32_bf16 v[200:203], v[20:23], v[160:163], v[200:203]
	v_mfma_f32_16x16x32_bf16 v[204:207], v[24:27], v[160:163], v[204:207]
	v_mfma_f32_16x16x32_bf16 v[208:211], v[28:31], v[160:163], v[208:211]
	v_mfma_f32_16x16x32_bf16 v[212:215], v[32:35], v[160:163], v[212:215]
	ds_read2_b64 v[20:23], v11 offset0:32 offset1:36
	ds_read2_b64 v[24:27], v12 offset0:32 offset1:36
	ds_read2_b64 v[28:31], v13 offset0:32 offset1:36
	ds_read2_b64 v[32:35], v14 offset0:32 offset1:36
	s_waitcnt lgkmcnt(6)
	v_mfma_f32_16x16x32_bf16 v[184:187], v[36:39], v[132:135], v[184:187]
	v_mfma_f32_16x16x32_bf16 v[188:191], v[40:43], v[132:135], v[188:191]
	v_mfma_f32_16x16x32_bf16 v[192:195], v[44:47], v[132:135], v[192:195]
	v_mfma_f32_16x16x32_bf16 v[196:199], v[48:51], v[132:135], v[196:199]
	v_mfma_f32_16x16x32_bf16 v[200:203], v[36:39], v[168:171], v[200:203]
	v_mfma_f32_16x16x32_bf16 v[204:207], v[40:43], v[168:171], v[204:207]
	v_mfma_f32_16x16x32_bf16 v[208:211], v[44:47], v[168:171], v[208:211]
	v_mfma_f32_16x16x32_bf16 v[212:215], v[48:51], v[168:171], v[212:215]
	s_waitcnt lgkmcnt(0)
	v_mfma_f32_16x16x32_bf16 v[184:187], v[20:23], v[140:143], v[184:187]
	v_mfma_f32_16x16x32_bf16 v[188:191], v[24:27], v[140:143], v[188:191]
	v_mfma_f32_16x16x32_bf16 v[192:195], v[28:31], v[140:143], v[192:195]
	v_mfma_f32_16x16x32_bf16 v[196:199], v[32:35], v[140:143], v[196:199]
	v_mfma_f32_16x16x32_bf16 v[200:203], v[20:23], v[176:179], v[200:203]
	v_mfma_f32_16x16x32_bf16 v[204:207], v[24:27], v[176:179], v[204:207]
	v_mfma_f32_16x16x32_bf16 v[208:211], v[28:31], v[176:179], v[208:211]
	v_mfma_f32_16x16x32_bf16 v[212:215], v[32:35], v[176:179], v[212:215]
	v_add_f32_e32 v232, v232, v233
	v_add_f32_e32 v226, v226, v227
	v_add_f32_e32 v232, v232, v88
	v_add_f32_e32 v226, v226, v88
	v_rcp_f32_e32 v236, v232
	v_rcp_f32_e32 v230, v226
	v_mov_b32_e32 v237, v236
	v_mov_b32_e32 v231, v230
	s_nop 1
	v_pk_mul_f32 v[184:185], v[184:185], v[236:237]
	v_pk_mul_f32 v[186:187], v[186:187], v[236:237]
	v_pk_mul_f32 v[188:189], v[188:189], v[236:237]
	v_pk_mul_f32 v[190:191], v[190:191], v[236:237]
	v_pk_mul_f32 v[192:193], v[192:193], v[236:237]
	v_pk_mul_f32 v[194:195], v[194:195], v[236:237]
	v_pk_mul_f32 v[196:197], v[196:197], v[236:237]
	v_pk_mul_f32 v[198:199], v[198:199], v[236:237]
	v_pk_mul_f32 v[200:201], v[200:201], v[230:231]
	v_pk_mul_f32 v[202:203], v[202:203], v[230:231]
	v_pk_mul_f32 v[204:205], v[204:205], v[230:231]
	v_pk_mul_f32 v[206:207], v[206:207], v[230:231]
	v_pk_mul_f32 v[208:209], v[208:209], v[230:231]
	v_pk_mul_f32 v[210:211], v[210:211], v[230:231]
	v_pk_mul_f32 v[212:213], v[212:213], v[230:231]
	v_pk_mul_f32 v[214:215], v[214:215], v[230:231]
	v_cvt_pk_bf16_f32 v184, v184, v185
	v_cvt_pk_bf16_f32 v185, v186, v187
	v_cvt_pk_bf16_f32 v188, v188, v189
	v_cvt_pk_bf16_f32 v189, v190, v191
	v_cvt_pk_bf16_f32 v192, v192, v193
	v_cvt_pk_bf16_f32 v193, v194, v195
	v_cvt_pk_bf16_f32 v196, v196, v197
	v_cvt_pk_bf16_f32 v197, v198, v199
	v_cvt_pk_bf16_f32 v200, v200, v201
	v_cvt_pk_bf16_f32 v201, v202, v203
	v_cvt_pk_bf16_f32 v204, v204, v205
	v_cvt_pk_bf16_f32 v205, v206, v207
	v_cvt_pk_bf16_f32 v208, v208, v209
	v_cvt_pk_bf16_f32 v209, v210, v211
	v_cvt_pk_bf16_f32 v212, v212, v213
	v_cvt_pk_bf16_f32 v213, v214, v215
	global_store_dwordx2 v9, v[184:185], s[50:51] offset:0
	global_store_dwordx2 v9, v[188:189], s[50:51] offset:32
	global_store_dwordx2 v9, v[192:193], s[50:51] offset:64
	global_store_dwordx2 v9, v[196:197], s[50:51] offset:96
	global_store_dwordx2 v9, v[200:201], s[60:61] offset:0
	global_store_dwordx2 v9, v[204:205], s[60:61] offset:32
	global_store_dwordx2 v9, v[208:209], s[60:61] offset:64
	global_store_dwordx2 v9, v[212:213], s[60:61] offset:96
	s_add_u32 s50, s50, 0x20000
	s_addc_u32 s51, s51, 0
	s_add_u32 s60, s60, 0x20000
	s_addc_u32 s61, s61, 0
	ds_read_b128 v[20:23], v10 offset:4608
	ds_read_b128 v[24:27], v10 offset:4672
	ds_read_b128 v[28:31], v10 offset:6912
	ds_read_b128 v[32:35], v10 offset:6976
	ds_read_b128 v[36:39], v10 offset:9216
	ds_read_b128 v[40:43], v10 offset:9280
	ds_read_b128 v[44:47], v10 offset:11520
	ds_read_b128 v[48:51], v10 offset:11584
	ds_read_b128 v[216:219], v10 offset:13824
	ds_read_b128 v[220:223], v10 offset:13888
	s_waitcnt vmcnt(8)
	v_lshlrev_b32_e32 v234, 16, v92
	v_and_b32_e32 v235, 0xffff0000, v92
	v_pk_mul_f32 v[232:233], v[234:235], v[234:235]
	v_lshlrev_b32_e32 v228, 16, v100
	v_and_b32_e32 v229, 0xffff0000, v100
	v_pk_mul_f32 v[226:227], v[228:229], v[228:229]
	v_lshlrev_b32_e32 v234, 16, v93
	v_and_b32_e32 v235, 0xffff0000, v93
	v_pk_fma_f32 v[232:233], v[234:235], v[234:235], v[232:233]
	v_lshlrev_b32_e32 v228, 16, v101
	v_and_b32_e32 v229, 0xffff0000, v101
	v_pk_fma_f32 v[226:227], v[228:229], v[228:229], v[226:227]
	v_lshlrev_b32_e32 v234, 16, v94
	v_and_b32_e32 v235, 0xffff0000, v94
	v_pk_fma_f32 v[232:233], v[234:235], v[234:235], v[232:233]
	v_lshlrev_b32_e32 v228, 16, v102
	v_and_b32_e32 v229, 0xffff0000, v102
	v_pk_fma_f32 v[226:227], v[228:229], v[228:229], v[226:227]
	v_lshlrev_b32_e32 v234, 16, v95
	v_and_b32_e32 v235, 0xffff0000, v95
	v_pk_fma_f32 v[232:233], v[234:235], v[234:235], v[232:233]
	v_lshlrev_b32_e32 v228, 16, v103
	v_and_b32_e32 v229, 0xffff0000, v103
	v_pk_fma_f32 v[226:227], v[228:229], v[228:229], v[226:227]
	v_lshlrev_b32_e32 v234, 16, v96
	v_and_b32_e32 v235, 0xffff0000, v96
	v_pk_fma_f32 v[232:233], v[234:235], v[234:235], v[232:233]
	v_lshlrev_b32_e32 v228, 16, v104
	v_and_b32_e32 v229, 0xffff0000, v104
	v_pk_fma_f32 v[226:227], v[228:229], v[228:229], v[226:227]
	v_lshlrev_b32_e32 v234, 16, v97
	v_and_b32_e32 v235, 0xffff0000, v97
	v_pk_fma_f32 v[232:233], v[234:235], v[234:235], v[232:233]
	v_lshlrev_b32_e32 v228, 16, v105
	v_and_b32_e32 v229, 0xffff0000, v105
	v_pk_fma_f32 v[226:227], v[228:229], v[228:229], v[226:227]
	v_lshlrev_b32_e32 v234, 16, v98
	v_and_b32_e32 v235, 0xffff0000, v98
	v_pk_fma_f32 v[232:233], v[234:235], v[234:235], v[232:233]
	v_lshlrev_b32_e32 v228, 16, v106
	v_and_b32_e32 v229, 0xffff0000, v106
	v_pk_fma_f32 v[226:227], v[228:229], v[228:229], v[226:227]
	v_lshlrev_b32_e32 v234, 16, v99
	v_and_b32_e32 v235, 0xffff0000, v99
	v_pk_fma_f32 v[232:233], v[234:235], v[234:235], v[232:233]
	v_lshlrev_b32_e32 v228, 16, v107
	v_and_b32_e32 v229, 0xffff0000, v107
	v_pk_fma_f32 v[226:227], v[228:229], v[228:229], v[226:227]
	v_add_f32_e32 v232, v232, v233
	v_add_f32_e32 v226, v226, v227
	s_nop 0
	ds_bpermute_b32 v233, v15, v232
	ds_bpermute_b32 v227, v15, v226
	s_waitcnt lgkmcnt(6)
	v_mfma_f32_16x16x32_bf16 v[108:111], v[20:23], v[92:95], 0
	v_mfma_f32_16x16x32_bf16 v[112:115], v[28:31], v[92:95], 0
	v_mfma_f32_16x16x32_bf16 v[148:151], v[28:31], v[100:103], 0
	v_mfma_f32_16x16x32_bf16 v[116:119], v[36:39], v[92:95], 0
	v_mfma_f32_16x16x32_bf16 v[152:155], v[36:39], v[100:103], 0
	v_mfma_f32_16x16x32_bf16 v[108:111], v[24:27], v[96:99], v[108:111]
	v_mfma_f32_16x16x32_bf16 v[112:115], v[32:35], v[96:99], v[112:115]
	v_mfma_f32_16x16x32_bf16 v[148:151], v[32:35], v[104:107], v[148:151]
	v_mfma_f32_16x16x32_bf16 v[116:119], v[40:43], v[96:99], v[116:119]
	v_mfma_f32_16x16x32_bf16 v[152:155], v[40:43], v[104:107], v[152:155]
	ds_read_b128 v[20:23], v10 offset:16128
	ds_read_b128 v[24:27], v10 offset:16192
	ds_read_b128 v[28:31], v10 offset:18432
	ds_read_b128 v[32:35], v10 offset:18496
	ds_read_b128 v[36:39], v10 offset:20736
	ds_read_b128 v[40:43], v10 offset:20800
	s_waitcnt lgkmcnt(6)
	v_add_f32_e32 v232, v232, v233
	v_add_f32_e32 v226, v226, v227
	s_nop 0
	ds_bpermute_b32 v233, v16, v232
	ds_bpermute_b32 v227, v16, v226
	v_mfma_f32_16x16x32_bf16 v[120:123], v[44:47], v[92:95], 0
	v_mfma_f32_16x16x32_bf16 v[156:159], v[44:47], v[100:103], 0
	v_mfma_f32_16x16x32_bf16 v[124:127], v[216:219], v[92:95], 0
	v_mfma_f32_16x16x32_bf16 v[160:163], v[216:219], v[100:103], 0
	v_mfma_f32_16x16x32_bf16 v[120:123], v[48:51], v[96:99], v[120:123]
	v_mfma_f32_16x16x32_bf16 v[156:159], v[48:51], v[104:107], v[156:159]
	v_mfma_f32_16x16x32_bf16 v[124:127], v[220:223], v[96:99], v[124:127]
	v_mfma_f32_16x16x32_bf16 v[160:163], v[220:223], v[104:107], v[160:163]
	ds_read_b128 v[44:47], v10 offset:23040
	ds_read_b128 v[48:51], v10 offset:23104
	ds_read_b128 v[216:219], v10 offset:25344
	ds_read_b128 v[220:223], v10 offset:25408
	s_waitcnt lgkmcnt(6)
	v_mfma_f32_16x16x32_bf16 v[128:131], v[20:23], v[92:95], 0
	v_mfma_f32_16x16x32_bf16 v[164:167], v[20:23], v[100:103], 0
	v_mfma_f32_16x16x32_bf16 v[132:135], v[28:31], v[92:95], 0
	v_mfma_f32_16x16x32_bf16 v[168:171], v[28:31], v[100:103], 0
	v_mfma_f32_16x16x32_bf16 v[136:139], v[36:39], v[92:95], 0
	v_mfma_f32_16x16x32_bf16 v[172:175], v[36:39], v[100:103], 0
	v_mfma_f32_16x16x32_bf16 v[128:131], v[24:27], v[96:99], v[128:131]
	v_mfma_f32_16x16x32_bf16 v[164:167], v[24:27], v[104:107], v[164:167]
	v_mfma_f32_16x16x32_bf16 v[132:135], v[32:35], v[96:99], v[132:135]
	v_mfma_f32_16x16x32_bf16 v[168:171], v[32:35], v[104:107], v[168:171]
	v_mfma_f32_16x16x32_bf16 v[136:139], v[40:43], v[96:99], v[136:139]
	v_mfma_f32_16x16x32_bf16 v[172:175], v[40:43], v[104:107], v[172:175]
	s_waitcnt lgkmcnt(0)
	v_mfma_f32_16x16x32_bf16 v[140:143], v[44:47], v[92:95], 0
	v_mfma_f32_16x16x32_bf16 v[176:179], v[44:47], v[100:103], 0
	v_mfma_f32_16x16x32_bf16 v[180:183], v[216:219], v[100:103], 0
	v_mfma_f32_16x16x32_bf16 v[140:143], v[48:51], v[96:99], v[140:143]
	v_mfma_f32_16x16x32_bf16 v[176:179], v[48:51], v[104:107], v[176:179]
	v_mfma_f32_16x16x32_bf16 v[180:183], v[220:223], v[104:107], v[180:183]
	s_add_u32 s48, s48, 0x28000
	s_addc_u32 s49, s49, 0
	s_add_u32 s58, s58, 0x28000
	s_addc_u32 s59, s59, 0
	global_load_dwordx4 v[92:95], v8, s[48:49]
	global_load_dwordx4 v[96:99], v8, s[48:49] offset:64
	global_load_dwordx4 v[100:103], v8, s[58:59]
	global_load_dwordx4 v[104:107], v8, s[58:59] offset:64
	ds_read2_b64 v[20:23], v11 offset0:8 offset1:12
	ds_read2_b64 v[24:27], v12 offset0:8 offset1:12
	ds_read2_b64 v[28:31], v13 offset0:8 offset1:12
	ds_read2_b64 v[32:35], v14 offset0:8 offset1:12
	ds_read2_b64 v[36:39], v11 offset0:16 offset1:20
	ds_read2_b64 v[40:43], v12 offset0:16 offset1:20
	ds_read2_b64 v[44:47], v13 offset0:16 offset1:20
	ds_read2_b64 v[48:51], v14 offset0:16 offset1:20
	v_add_f32_e32 v232, v232, v233
	v_add_f32_e32 v226, v226, v227
	v_mul_f32_e32 v232, 0x3c800000, v232
	v_mul_f32_e32 v226, 0x3c800000, v226
	v_add_f32_e32 v232, 0x358637bd, v232
	v_add_f32_e32 v226, 0x358637bd, v226
	v_rsq_f32_e32 v236, v232
	v_rsq_f32_e32 v230, v226
	v_mov_b32_e32 v237, v236
	v_mov_b32_e32 v231, v230
	s_nop 1
	v_pk_fma_f32 v[108:109], v[108:109], v[236:237], v[52:53]
	v_pk_fma_f32 v[110:111], v[110:111], v[236:237], v[54:55]
	v_pk_fma_f32 v[148:149], v[148:149], v[230:231], v[52:53]
	v_pk_fma_f32 v[150:151], v[150:151], v[230:231], v[54:55]
	v_pk_fma_f32 v[112:113], v[112:113], v[236:237], v[56:57]
	v_pk_fma_f32 v[114:115], v[114:115], v[236:237], v[58:59]
	v_pk_fma_f32 v[152:153], v[152:153], v[230:231], v[56:57]
	v_pk_fma_f32 v[154:155], v[154:155], v[230:231], v[58:59]
	v_pk_fma_f32 v[116:117], v[116:117], v[236:237], v[60:61]
	v_pk_fma_f32 v[118:119], v[118:119], v[236:237], v[62:63]
	v_pk_fma_f32 v[156:157], v[156:157], v[230:231], v[60:61]
	v_pk_fma_f32 v[158:159], v[158:159], v[230:231], v[62:63]
	v_pk_fma_f32 v[120:121], v[120:121], v[236:237], v[64:65]
	v_pk_fma_f32 v[122:123], v[122:123], v[236:237], v[66:67]
	v_pk_fma_f32 v[160:161], v[160:161], v[230:231], v[64:65]
	v_pk_fma_f32 v[162:163], v[162:163], v[230:231], v[66:67]
	v_pk_fma_f32 v[124:125], v[124:125], v[236:237], v[68:69]
	v_pk_fma_f32 v[126:127], v[126:127], v[236:237], v[70:71]
	v_pk_fma_f32 v[164:165], v[164:165], v[230:231], v[68:69]
	v_pk_fma_f32 v[166:167], v[166:167], v[230:231], v[70:71]
	v_pk_fma_f32 v[128:129], v[128:129], v[236:237], v[72:73]
	v_pk_fma_f32 v[130:131], v[130:131], v[236:237], v[74:75]
	v_pk_fma_f32 v[168:169], v[168:169], v[230:231], v[72:73]
	v_pk_fma_f32 v[170:171], v[170:171], v[230:231], v[74:75]
	v_pk_fma_f32 v[132:133], v[132:133], v[236:237], v[76:77]
	v_pk_fma_f32 v[134:135], v[134:135], v[236:237], v[78:79]
	v_pk_fma_f32 v[172:173], v[172:173], v[230:231], v[76:77]
	v_pk_fma_f32 v[174:175], v[174:175], v[230:231], v[78:79]
	v_pk_fma_f32 v[136:137], v[136:137], v[236:237], v[80:81]
	v_pk_fma_f32 v[138:139], v[138:139], v[236:237], v[82:83]
	v_pk_fma_f32 v[176:177], v[176:177], v[230:231], v[80:81]
	v_pk_fma_f32 v[178:179], v[178:179], v[230:231], v[82:83]
	v_pk_fma_f32 v[140:141], v[140:141], v[236:237], v[84:85]
	v_pk_fma_f32 v[142:143], v[142:143], v[236:237], v[86:87]
	v_pk_fma_f32 v[180:181], v[180:181], v[230:231], v[84:85]
	v_pk_fma_f32 v[182:183], v[182:183], v[230:231], v[86:87]
	v_exp_f32_e32 v108, v108
	v_exp_f32_e32 v109, v109
	v_exp_f32_e32 v110, v110
	v_exp_f32_e32 v111, v111
	v_exp_f32_e32 v148, v148
	v_exp_f32_e32 v149, v149
	v_exp_f32_e32 v150, v150
	v_exp_f32_e32 v151, v151
	v_exp_f32_e32 v112, v112
	v_exp_f32_e32 v113, v113
	v_exp_f32_e32 v114, v114
	v_exp_f32_e32 v115, v115
	v_exp_f32_e32 v152, v152
	v_exp_f32_e32 v153, v153
	v_exp_f32_e32 v154, v154
	v_exp_f32_e32 v155, v155
	v_exp_f32_e32 v116, v116
	v_exp_f32_e32 v117, v117
	v_exp_f32_e32 v118, v118
	v_exp_f32_e32 v119, v119
	v_exp_f32_e32 v156, v156
	v_exp_f32_e32 v157, v157
	v_exp_f32_e32 v158, v158
	v_exp_f32_e32 v159, v159
	v_exp_f32_e32 v120, v120
	v_exp_f32_e32 v121, v121
	v_exp_f32_e32 v122, v122
	v_exp_f32_e32 v123, v123
	v_exp_f32_e32 v160, v160
	v_exp_f32_e32 v161, v161
	v_exp_f32_e32 v162, v162
	v_exp_f32_e32 v163, v163
	v_exp_f32_e32 v124, v124
	v_exp_f32_e32 v125, v125
	v_exp_f32_e32 v126, v126
	v_exp_f32_e32 v127, v127
	v_exp_f32_e32 v164, v164
	v_exp_f32_e32 v165, v165
	v_exp_f32_e32 v166, v166
	v_exp_f32_e32 v167, v167
	v_exp_f32_e32 v128, v128
	v_exp_f32_e32 v129, v129
	v_exp_f32_e32 v130, v130
	v_exp_f32_e32 v131, v131
	v_exp_f32_e32 v168, v168
	v_exp_f32_e32 v169, v169
	v_exp_f32_e32 v170, v170
	v_exp_f32_e32 v171, v171
	v_exp_f32_e32 v132, v132
	v_exp_f32_e32 v133, v133
	v_exp_f32_e32 v134, v134
	v_exp_f32_e32 v135, v135
	v_exp_f32_e32 v172, v172
	v_exp_f32_e32 v173, v173
	v_exp_f32_e32 v174, v174
	v_exp_f32_e32 v175, v175
	v_exp_f32_e32 v136, v136
	v_exp_f32_e32 v137, v137
	v_exp_f32_e32 v138, v138
	v_exp_f32_e32 v139, v139
	v_exp_f32_e32 v176, v176
	v_exp_f32_e32 v177, v177
	v_exp_f32_e32 v178, v178
	v_exp_f32_e32 v179, v179
	v_exp_f32_e32 v140, v140
	v_exp_f32_e32 v141, v141
	v_exp_f32_e32 v142, v142
	v_exp_f32_e32 v143, v143
	v_exp_f32_e32 v180, v180
	v_exp_f32_e32 v181, v181
	v_exp_f32_e32 v182, v182
	v_exp_f32_e32 v183, v183
	s_cmp_lg_u32 s36, 0
	s_cbranch_scc1 .Lat_m1
	v_mov_b32_e32 v108, 0
	v_mov_b32_e32 v109, 0
	v_mov_b32_e32 v110, 0
	v_mov_b32_e32 v111, 0
	v_mov_b32_e32 v112, 0
	v_mov_b32_e32 v113, 0
	v_mov_b32_e32 v114, 0
	v_mov_b32_e32 v115, 0
	v_mov_b32_e32 v116, 0
	v_mov_b32_e32 v117, 0
	v_mov_b32_e32 v118, 0
	v_mov_b32_e32 v119, 0
	v_mov_b32_e32 v120, 0
	v_mov_b32_e32 v121, 0
	v_mov_b32_e32 v122, 0
	v_mov_b32_e32 v123, 0
	v_mov_b32_e32 v124, 0
	v_mov_b32_e32 v125, 0
	v_mov_b32_e32 v126, 0
	v_mov_b32_e32 v127, 0
	v_mov_b32_e32 v128, 0
	v_mov_b32_e32 v129, 0
	v_mov_b32_e32 v130, 0
	v_mov_b32_e32 v131, 0
	v_mov_b32_e32 v148, 0
	v_mov_b32_e32 v149, 0
	v_mov_b32_e32 v150, 0
	v_mov_b32_e32 v151, 0
	v_mov_b32_e32 v152, 0
	v_mov_b32_e32 v153, 0
	v_mov_b32_e32 v154, 0
	v_mov_b32_e32 v155, 0
	v_mov_b32_e32 v156, 0
	v_mov_b32_e32 v157, 0
	v_mov_b32_e32 v158, 0
	v_mov_b32_e32 v159, 0
	v_mov_b32_e32 v160, 0
	v_mov_b32_e32 v161, 0
	v_mov_b32_e32 v162, 0
	v_mov_b32_e32 v163, 0
	v_mov_b32_e32 v164, 0
	v_mov_b32_e32 v165, 0
	v_mov_b32_e32 v166, 0
	v_mov_b32_e32 v167, 0
.Lat_m1:
	s_nop 0
	v_pk_add_f32 v[232:233], v[108:109], v[110:111]
	v_pk_add_f32 v[234:235], v[112:113], v[114:115]
	v_pk_add_f32 v[226:227], v[148:149], v[150:151]
	v_pk_add_f32 v[228:229], v[152:153], v[154:155]
	v_pk_add_f32 v[232:233], v[232:233], v[116:117]
	v_pk_add_f32 v[234:235], v[234:235], v[118:119]
	v_pk_add_f32 v[226:227], v[226:227], v[156:157]
	v_pk_add_f32 v[228:229], v[228:229], v[158:159]
	v_pk_add_f32 v[232:233], v[232:233], v[120:121]
	v_pk_add_f32 v[234:235], v[234:235], v[122:123]
	v_pk_add_f32 v[226:227], v[226:227], v[160:161]
	v_pk_add_f32 v[228:229], v[228:229], v[162:163]
	v_pk_add_f32 v[232:233], v[232:233], v[124:125]
	v_pk_add_f32 v[234:235], v[234:235], v[126:127]
	v_pk_add_f32 v[226:227], v[226:227], v[164:165]
	v_pk_add_f32 v[228:229], v[228:229], v[166:167]
	v_pk_add_f32 v[232:233], v[232:233], v[128:129]
	v_pk_add_f32 v[234:235], v[234:235], v[130:131]
	v_pk_add_f32 v[226:227], v[226:227], v[168:169]
	v_pk_add_f32 v[228:229], v[228:229], v[170:171]
	v_pk_add_f32 v[232:233], v[232:233], v[132:133]
	v_pk_add_f32 v[234:235], v[234:235], v[134:135]
	v_pk_add_f32 v[226:227], v[226:227], v[172:173]
	v_pk_add_f32 v[228:229], v[228:229], v[174:175]
	v_pk_add_f32 v[232:233], v[232:233], v[136:137]
	v_pk_add_f32 v[234:235], v[234:235], v[138:139]
	v_pk_add_f32 v[226:227], v[226:227], v[176:177]
	v_pk_add_f32 v[228:229], v[228:229], v[178:179]
	v_pk_add_f32 v[232:233], v[232:233], v[140:141]
	v_pk_add_f32 v[234:235], v[234:235], v[142:143]
	v_pk_add_f32 v[226:227], v[226:227], v[180:181]
	v_pk_add_f32 v[228:229], v[228:229], v[182:183]
	v_pk_add_f32 v[232:233], v[232:233], v[234:235]
	v_pk_add_f32 v[226:227], v[226:227], v[228:229]
	v_add_f32_e32 v232, v232, v233
	v_add_f32_e32 v226, v226, v227
	v_cvt_pk_bf16_f32 v108, v108, v109
	v_cvt_pk_bf16_f32 v109, v110, v111
	v_cvt_pk_bf16_f32 v110, v112, v113
	v_cvt_pk_bf16_f32 v111, v114, v115
	v_cvt_pk_bf16_f32 v146, v148, v149
	v_cvt_pk_bf16_f32 v147, v150, v151
	v_cvt_pk_bf16_f32 v116, v116, v117
	v_cvt_pk_bf16_f32 v117, v118, v119
	v_cvt_pk_bf16_f32 v118, v120, v121
	v_cvt_pk_bf16_f32 v119, v122, v123
	v_cvt_pk_bf16_f32 v152, v152, v153
	v_cvt_pk_bf16_f32 v153, v154, v155
	v_cvt_pk_bf16_f32 v154, v156, v157
	v_cvt_pk_bf16_f32 v155, v158, v159
	v_cvt_pk_bf16_f32 v124, v124, v125
	v_cvt_pk_bf16_f32 v125, v126, v127
	v_cvt_pk_bf16_f32 v126, v128, v129
	v_cvt_pk_bf16_f32 v127, v130, v131
	v_cvt_pk_bf16_f32 v160, v160, v161
	v_cvt_pk_bf16_f32 v161, v162, v163
	v_cvt_pk_bf16_f32 v162, v164, v165
	v_cvt_pk_bf16_f32 v163, v166, v167
	v_cvt_pk_bf16_f32 v132, v132, v133
	v_cvt_pk_bf16_f32 v133, v134, v135
	v_cvt_pk_bf16_f32 v134, v136, v137
	v_cvt_pk_bf16_f32 v135, v138, v139
	v_cvt_pk_bf16_f32 v168, v168, v169
	v_cvt_pk_bf16_f32 v169, v170, v171
	v_cvt_pk_bf16_f32 v170, v172, v173
	v_cvt_pk_bf16_f32 v171, v174, v175
	v_cvt_pk_bf16_f32 v140, v140, v141
	v_cvt_pk_bf16_f32 v141, v142, v143
	v_mov_b32_e32 v142, 0
	v_mov_b32_e32 v143, 0
	v_cvt_pk_bf16_f32 v176, v176, v177
	v_cvt_pk_bf16_f32 v177, v178, v179
	v_cvt_pk_bf16_f32 v178, v180, v181
	v_cvt_pk_bf16_f32 v179, v182, v183
	ds_bpermute_b32 v233, v15, v232
	ds_bpermute_b32 v227, v15, v226
	s_waitcnt lgkmcnt(2)
	v_mfma_f32_16x16x32_bf16 v[184:187], v[20:23], v[108:111], 0
	v_mfma_f32_16x16x32_bf16 v[188:191], v[24:27], v[108:111], 0
	v_mfma_f32_16x16x32_bf16 v[192:195], v[28:31], v[108:111], 0
	v_mfma_f32_16x16x32_bf16 v[196:199], v[32:35], v[108:111], 0
	v_mfma_f32_16x16x32_bf16 v[200:203], v[20:23], v[144:147], 0
	v_mfma_f32_16x16x32_bf16 v[204:207], v[24:27], v[144:147], 0
	v_mfma_f32_16x16x32_bf16 v[208:211], v[28:31], v[144:147], 0
	v_mfma_f32_16x16x32_bf16 v[212:215], v[32:35], v[144:147], 0
	ds_read2_b64 v[20:23], v11 offset0:24 offset1:28
	ds_read2_b64 v[24:27], v12 offset0:24 offset1:28
	ds_read2_b64 v[28:31], v13 offset0:24 offset1:28
	ds_read2_b64 v[32:35], v14 offset0:24 offset1:28
	v_mfma_f32_16x16x32_bf16 v[184:187], v[36:39], v[116:119], v[184:187]
	v_mfma_f32_16x16x32_bf16 v[188:191], v[40:43], v[116:119], v[188:191]
	v_mfma_f32_16x16x32_bf16 v[192:195], v[44:47], v[116:119], v[192:195]
	v_mfma_f32_16x16x32_bf16 v[196:199], v[48:51], v[116:119], v[196:199]
	v_mfma_f32_16x16x32_bf16 v[200:203], v[36:39], v[152:155], v[200:203]
	v_mfma_f32_16x16x32_bf16 v[204:207], v[40:43], v[152:155], v[204:207]
	v_mfma_f32_16x16x32_bf16 v[208:211], v[44:47], v[152:155], v[208:211]
	v_mfma_f32_16x16x32_bf16 v[212:215], v[48:51], v[152:155], v[212:215]
	ds_read2_b64 v[36:39], v11 offset0:32 offset1:36
	ds_read2_b64 v[40:43], v12 offset0:32 offset1:36
	ds_read2_b64 v[44:47], v13 offset0:32 offset1:36
	ds_read2_b64 v[48:51], v14 offset0:32 offset1:36
	s_waitcnt lgkmcnt(8)
	v_add_f32_e32 v232, v232, v233
	v_add_f32_e32 v226, v226, v227
	s_nop 0
	ds_bpermute_b32 v233, v16, v232
	ds_bpermute_b32 v227, v16, v226
	s_waitcnt lgkmcnt(6)
	v_mfma_f32_16x16x32_bf16 v[184:187], v[20:23], v[124:127], v[184:187]
	v_mfma_f32_16x16x32_bf16 v[188:191], v[24:27], v[124:127], v[188:191]
	v_mfma_f32_16x16x32_bf16 v[192:195], v[28:31], v[124:127], v[192:195]
	v_mfma_f32_16x16x32_bf16 v[196:199], v[32:35], v[124:127], v[196:199]
	v_mfma_f32_16x16x32_bf16 v[200:203], v[20:23], v[160:163], v[200:203]
	v_mfma_f32_16x16x32_bf16 v[204:207], v[24:27], v[160:163], v[204:207]
	v_mfma_f32_16x16x32_bf16 v[208:211], v[28:31], v[160:163], v[208:211]
	v_mfma_f32_16x16x32_bf16 v[212:215], v[32:35], v[160:163], v[212:215]
	ds_read2_b64 v[20:23], v11 offset0:40 offset1:44
	ds_read2_b64 v[24:27], v12 offset0:40 offset1:44
	ds_read2_b64 v[28:31], v13 offset0:40 offset1:44
	ds_read2_b64 v[32:35], v14 offset0:40 offset1:44
	s_waitcnt lgkmcnt(6)
	v_mfma_f32_16x16x32_bf16 v[184:187], v[36:39], v[132:135], v[184:187]
	v_mfma_f32_16x16x32_bf16 v[188:191], v[40:43], v[132:135], v[188:191]
	v_mfma_f32_16x16x32_bf16 v[192:195], v[44:47], v[132:135], v[192:195]
	v_mfma_f32_16x16x32_bf16 v[196:199], v[48:51], v[132:135], v[196:199]
	v_mfma_f32_16x16x32_bf16 v[200:203], v[36:39], v[168:171], v[200:203]
	v_mfma_f32_16x16x32_bf16 v[204:207], v[40:43], v[168:171], v[204:207]
	v_mfma_f32_16x16x32_bf16 v[208:211], v[44:47], v[168:171], v[208:211]
	v_mfma_f32_16x16x32_bf16 v[212:215], v[48:51], v[168:171], v[212:215]
	s_waitcnt lgkmcnt(0)
	v_mfma_f32_16x16x32_bf16 v[184:187], v[20:23], v[140:143], v[184:187]
	v_mfma_f32_16x16x32_bf16 v[188:191], v[24:27], v[140:143], v[188:191]
	v_mfma_f32_16x16x32_bf16 v[192:195], v[28:31], v[140:143], v[192:195]
	v_mfma_f32_16x16x32_bf16 v[196:199], v[32:35], v[140:143], v[196:199]
	v_mfma_f32_16x16x32_bf16 v[200:203], v[20:23], v[176:179], v[200:203]
	v_mfma_f32_16x16x32_bf16 v[204:207], v[24:27], v[176:179], v[204:207]
	v_mfma_f32_16x16x32_bf16 v[208:211], v[28:31], v[176:179], v[208:211]
	v_mfma_f32_16x16x32_bf16 v[212:215], v[32:35], v[176:179], v[212:215]
	v_add_f32_e32 v232, v232, v233
	v_add_f32_e32 v226, v226, v227
	v_add_f32_e32 v232, v232, v88
	v_add_f32_e32 v226, v226, v88
	v_rcp_f32_e32 v236, v232
	v_rcp_f32_e32 v230, v226
	v_mov_b32_e32 v237, v236
	v_mov_b32_e32 v231, v230
	s_nop 1
	v_pk_mul_f32 v[184:185], v[184:185], v[236:237]
	v_pk_mul_f32 v[186:187], v[186:187], v[236:237]
	v_pk_mul_f32 v[188:189], v[188:189], v[236:237]
	v_pk_mul_f32 v[190:191], v[190:191], v[236:237]
	v_pk_mul_f32 v[192:193], v[192:193], v[236:237]
	v_pk_mul_f32 v[194:195], v[194:195], v[236:237]
	v_pk_mul_f32 v[196:197], v[196:197], v[236:237]
	v_pk_mul_f32 v[198:199], v[198:199], v[236:237]
	v_pk_mul_f32 v[200:201], v[200:201], v[230:231]
	v_pk_mul_f32 v[202:203], v[202:203], v[230:231]
	v_pk_mul_f32 v[204:205], v[204:205], v[230:231]
	v_pk_mul_f32 v[206:207], v[206:207], v[230:231]
	v_pk_mul_f32 v[208:209], v[208:209], v[230:231]
	v_pk_mul_f32 v[210:211], v[210:211], v[230:231]
	v_pk_mul_f32 v[212:213], v[212:213], v[230:231]
	v_pk_mul_f32 v[214:215], v[214:215], v[230:231]
	v_cvt_pk_bf16_f32 v184, v184, v185
	v_cvt_pk_bf16_f32 v185, v186, v187
	v_cvt_pk_bf16_f32 v188, v188, v189
	v_cvt_pk_bf16_f32 v189, v190, v191
	v_cvt_pk_bf16_f32 v192, v192, v193
	v_cvt_pk_bf16_f32 v193, v194, v195
	v_cvt_pk_bf16_f32 v196, v196, v197
	v_cvt_pk_bf16_f32 v197, v198, v199
	v_cvt_pk_bf16_f32 v200, v200, v201
	v_cvt_pk_bf16_f32 v201, v202, v203
	v_cvt_pk_bf16_f32 v204, v204, v205
	v_cvt_pk_bf16_f32 v205, v206, v207
	v_cvt_pk_bf16_f32 v208, v208, v209
	v_cvt_pk_bf16_f32 v209, v210, v211
	v_cvt_pk_bf16_f32 v212, v212, v213
	v_cvt_pk_bf16_f32 v213, v214, v215
	global_store_dwordx2 v9, v[184:185], s[50:51] offset:0
	global_store_dwordx2 v9, v[188:189], s[50:51] offset:32
	global_store_dwordx2 v9, v[192:193], s[50:51] offset:64
	global_store_dwordx2 v9, v[196:197], s[50:51] offset:96
	global_store_dwordx2 v9, v[200:201], s[60:61] offset:0
	global_store_dwordx2 v9, v[204:205], s[60:61] offset:32
	global_store_dwordx2 v9, v[208:209], s[60:61] offset:64
	global_store_dwordx2 v9, v[212:213], s[60:61] offset:96
	s_add_u32 s50, s50, 0x20000
	s_addc_u32 s51, s51, 0
	s_add_u32 s60, s60, 0x20000
	s_addc_u32 s61, s61, 0
	ds_read_b128 v[20:23], v10 offset:9216
	ds_read_b128 v[24:27], v10 offset:9280
	ds_read_b128 v[28:31], v10 offset:11520
	ds_read_b128 v[32:35], v10 offset:11584
	ds_read_b128 v[36:39], v10 offset:13824
	ds_read_b128 v[40:43], v10 offset:13888
	ds_read_b128 v[44:47], v10 offset:16128
	ds_read_b128 v[48:51], v10 offset:16192
	ds_read_b128 v[216:219], v10 offset:18432
	ds_read_b128 v[220:223], v10 offset:18496
	s_waitcnt vmcnt(8)
	v_lshlrev_b32_e32 v234, 16, v92
	v_and_b32_e32 v235, 0xffff0000, v92
	v_pk_mul_f32 v[232:233], v[234:235], v[234:235]
	v_lshlrev_b32_e32 v228, 16, v100
	v_and_b32_e32 v229, 0xffff0000, v100
	v_pk_mul_f32 v[226:227], v[228:229], v[228:229]
	v_lshlrev_b32_e32 v234, 16, v93
	v_and_b32_e32 v235, 0xffff0000, v93
	v_pk_fma_f32 v[232:233], v[234:235], v[234:235], v[232:233]
	v_lshlrev_b32_e32 v228, 16, v101
	v_and_b32_e32 v229, 0xffff0000, v101
	v_pk_fma_f32 v[226:227], v[228:229], v[228:229], v[226:227]
	v_lshlrev_b32_e32 v234, 16, v94
	v_and_b32_e32 v235, 0xffff0000, v94
	v_pk_fma_f32 v[232:233], v[234:235], v[234:235], v[232:233]
	v_lshlrev_b32_e32 v228, 16, v102
	v_and_b32_e32 v229, 0xffff0000, v102
	v_pk_fma_f32 v[226:227], v[228:229], v[228:229], v[226:227]
	v_lshlrev_b32_e32 v234, 16, v95
	v_and_b32_e32 v235, 0xffff0000, v95
	v_pk_fma_f32 v[232:233], v[234:235], v[234:235], v[232:233]
	v_lshlrev_b32_e32 v228, 16, v103
	v_and_b32_e32 v229, 0xffff0000, v103
	v_pk_fma_f32 v[226:227], v[228:229], v[228:229], v[226:227]
	v_lshlrev_b32_e32 v234, 16, v96
	v_and_b32_e32 v235, 0xffff0000, v96
	v_pk_fma_f32 v[232:233], v[234:235], v[234:235], v[232:233]
	v_lshlrev_b32_e32 v228, 16, v104
	v_and_b32_e32 v229, 0xffff0000, v104
	v_pk_fma_f32 v[226:227], v[228:229], v[228:229], v[226:227]
	v_lshlrev_b32_e32 v234, 16, v97
	v_and_b32_e32 v235, 0xffff0000, v97
	v_pk_fma_f32 v[232:233], v[234:235], v[234:235], v[232:233]
	v_lshlrev_b32_e32 v228, 16, v105
	v_and_b32_e32 v229, 0xffff0000, v105
	v_pk_fma_f32 v[226:227], v[228:229], v[228:229], v[226:227]
	v_lshlrev_b32_e32 v234, 16, v98
	v_and_b32_e32 v235, 0xffff0000, v98
	v_pk_fma_f32 v[232:233], v[234:235], v[234:235], v[232:233]
	v_lshlrev_b32_e32 v228, 16, v106
	v_and_b32_e32 v229, 0xffff0000, v106
	v_pk_fma_f32 v[226:227], v[228:229], v[228:229], v[226:227]
	v_lshlrev_b32_e32 v234, 16, v99
	v_and_b32_e32 v235, 0xffff0000, v99
	v_pk_fma_f32 v[232:233], v[234:235], v[234:235], v[232:233]
	v_lshlrev_b32_e32 v228, 16, v107
	v_and_b32_e32 v229, 0xffff0000, v107
	v_pk_fma_f32 v[226:227], v[228:229], v[228:229], v[226:227]
	v_add_f32_e32 v232, v232, v233
	v_add_f32_e32 v226, v226, v227
	s_nop 0
	ds_bpermute_b32 v233, v15, v232
	ds_bpermute_b32 v227, v15, v226
	s_waitcnt lgkmcnt(6)
	v_mfma_f32_16x16x32_bf16 v[108:111], v[20:23], v[92:95], 0
	v_mfma_f32_16x16x32_bf16 v[112:115], v[28:31], v[92:95], 0
	v_mfma_f32_16x16x32_bf16 v[148:151], v[28:31], v[100:103], 0
	v_mfma_f32_16x16x32_bf16 v[116:119], v[36:39], v[92:95], 0
	v_mfma_f32_16x16x32_bf16 v[152:155], v[36:39], v[100:103], 0
	v_mfma_f32_16x16x32_bf16 v[108:111], v[24:27], v[96:99], v[108:111]
	v_mfma_f32_16x16x32_bf16 v[112:115], v[32:35], v[96:99], v[112:115]
	v_mfma_f32_16x16x32_bf16 v[148:151], v[32:35], v[104:107], v[148:151]
	v_mfma_f32_16x16x32_bf16 v[116:119], v[40:43], v[96:99], v[116:119]
	v_mfma_f32_16x16x32_bf16 v[152:155], v[40:43], v[104:107], v[152:155]
	ds_read_b128 v[20:23], v10 offset:20736
	ds_read_b128 v[24:27], v10 offset:20800
	ds_read_b128 v[28:31], v10 offset:23040
	ds_read_b128 v[32:35], v10 offset:23104
	ds_read_b128 v[36:39], v10 offset:25344
	ds_read_b128 v[40:43], v10 offset:25408
	s_waitcnt lgkmcnt(6)
	v_add_f32_e32 v232, v232, v233
	v_add_f32_e32 v226, v226, v227
	s_nop 0
	ds_bpermute_b32 v233, v16, v232
	ds_bpermute_b32 v227, v16, v226
	v_mfma_f32_16x16x32_bf16 v[120:123], v[44:47], v[92:95], 0
	v_mfma_f32_16x16x32_bf16 v[156:159], v[44:47], v[100:103], 0
	v_mfma_f32_16x16x32_bf16 v[124:127], v[216:219], v[92:95], 0
	v_mfma_f32_16x16x32_bf16 v[160:163], v[216:219], v[100:103], 0
	v_mfma_f32_16x16x32_bf16 v[120:123], v[48:51], v[96:99], v[120:123]
	v_mfma_f32_16x16x32_bf16 v[156:159], v[48:51], v[104:107], v[156:159]
	v_mfma_f32_16x16x32_bf16 v[124:127], v[220:223], v[96:99], v[124:127]
	v_mfma_f32_16x16x32_bf16 v[160:163], v[220:223], v[104:107], v[160:163]
	ds_read_b128 v[44:47], v10 offset:27648
	ds_read_b128 v[48:51], v10 offset:27712
	ds_read_b128 v[216:219], v10 offset:29952
	ds_read_b128 v[220:223], v10 offset:30016
	s_waitcnt lgkmcnt(6)
	v_mfma_f32_16x16x32_bf16 v[128:131], v[20:23], v[92:95], 0
	v_mfma_f32_16x16x32_bf16 v[164:167], v[20:23], v[100:103], 0
	v_mfma_f32_16x16x32_bf16 v[132:135], v[28:31], v[92:95], 0
	v_mfma_f32_16x16x32_bf16 v[168:171], v[28:31], v[100:103], 0
	v_mfma_f32_16x16x32_bf16 v[136:139], v[36:39], v[92:95], 0
	v_mfma_f32_16x16x32_bf16 v[172:175], v[36:39], v[100:103], 0
	v_mfma_f32_16x16x32_bf16 v[128:131], v[24:27], v[96:99], v[128:131]
	v_mfma_f32_16x16x32_bf16 v[164:167], v[24:27], v[104:107], v[164:167]
	v_mfma_f32_16x16x32_bf16 v[132:135], v[32:35], v[96:99], v[132:135]
	v_mfma_f32_16x16x32_bf16 v[168:171], v[32:35], v[104:107], v[168:171]
	v_mfma_f32_16x16x32_bf16 v[136:139], v[40:43], v[96:99], v[136:139]
	v_mfma_f32_16x16x32_bf16 v[172:175], v[40:43], v[104:107], v[172:175]
	s_waitcnt lgkmcnt(0)
	v_mfma_f32_16x16x32_bf16 v[140:143], v[44:47], v[92:95], 0
	v_mfma_f32_16x16x32_bf16 v[176:179], v[44:47], v[100:103], 0
	v_mfma_f32_16x16x32_bf16 v[180:183], v[216:219], v[100:103], 0
	v_mfma_f32_16x16x32_bf16 v[140:143], v[48:51], v[96:99], v[140:143]
	v_mfma_f32_16x16x32_bf16 v[176:179], v[48:51], v[104:107], v[176:179]
	v_mfma_f32_16x16x32_bf16 v[180:183], v[220:223], v[104:107], v[180:183]
	s_add_u32 s48, s48, 0x28000
	s_addc_u32 s49, s49, 0
	s_add_u32 s58, s58, 0x28000
	s_addc_u32 s59, s59, 0
	global_load_dwordx4 v[92:95], v8, s[48:49]
	global_load_dwordx4 v[96:99], v8, s[48:49] offset:64
	global_load_dwordx4 v[100:103], v8, s[58:59]
	global_load_dwordx4 v[104:107], v8, s[58:59] offset:64
	ds_read2_b64 v[20:23], v11 offset0:16 offset1:20
	ds_read2_b64 v[24:27], v12 offset0:16 offset1:20
	ds_read2_b64 v[28:31], v13 offset0:16 offset1:20
	ds_read2_b64 v[32:35], v14 offset0:16 offset1:20
	ds_read2_b64 v[36:39], v11 offset0:24 offset1:28
	ds_read2_b64 v[40:43], v12 offset0:24 offset1:28
	ds_read2_b64 v[44:47], v13 offset0:24 offset1:28
	ds_read2_b64 v[48:51], v14 offset0:24 offset1:28
	v_add_f32_e32 v232, v232, v233
	v_add_f32_e32 v226, v226, v227
	v_mul_f32_e32 v232, 0x3c800000, v232
	v_mul_f32_e32 v226, 0x3c800000, v226
	v_add_f32_e32 v232, 0x358637bd, v232
	v_add_f32_e32 v226, 0x358637bd, v226
	v_rsq_f32_e32 v236, v232
	v_rsq_f32_e32 v230, v226
	v_mov_b32_e32 v237, v236
	v_mov_b32_e32 v231, v230
	s_nop 1
	v_pk_fma_f32 v[108:109], v[108:109], v[236:237], v[52:53]
	v_pk_fma_f32 v[110:111], v[110:111], v[236:237], v[54:55]
	v_pk_fma_f32 v[148:149], v[148:149], v[230:231], v[52:53]
	v_pk_fma_f32 v[150:151], v[150:151], v[230:231], v[54:55]
	v_pk_fma_f32 v[112:113], v[112:113], v[236:237], v[56:57]
	v_pk_fma_f32 v[114:115], v[114:115], v[236:237], v[58:59]
	v_pk_fma_f32 v[152:153], v[152:153], v[230:231], v[56:57]
	v_pk_fma_f32 v[154:155], v[154:155], v[230:231], v[58:59]
	v_pk_fma_f32 v[116:117], v[116:117], v[236:237], v[60:61]
	v_pk_fma_f32 v[118:119], v[118:119], v[236:237], v[62:63]
	v_pk_fma_f32 v[156:157], v[156:157], v[230:231], v[60:61]
	v_pk_fma_f32 v[158:159], v[158:159], v[230:231], v[62:63]
	v_pk_fma_f32 v[120:121], v[120:121], v[236:237], v[64:65]
	v_pk_fma_f32 v[122:123], v[122:123], v[236:237], v[66:67]
	v_pk_fma_f32 v[160:161], v[160:161], v[230:231], v[64:65]
	v_pk_fma_f32 v[162:163], v[162:163], v[230:231], v[66:67]
	v_pk_fma_f32 v[124:125], v[124:125], v[236:237], v[68:69]
	v_pk_fma_f32 v[126:127], v[126:127], v[236:237], v[70:71]
	v_pk_fma_f32 v[164:165], v[164:165], v[230:231], v[68:69]
	v_pk_fma_f32 v[166:167], v[166:167], v[230:231], v[70:71]
	v_pk_fma_f32 v[128:129], v[128:129], v[236:237], v[72:73]
	v_pk_fma_f32 v[130:131], v[130:131], v[236:237], v[74:75]
	v_pk_fma_f32 v[168:169], v[168:169], v[230:231], v[72:73]
	v_pk_fma_f32 v[170:171], v[170:171], v[230:231], v[74:75]
	v_pk_fma_f32 v[132:133], v[132:133], v[236:237], v[76:77]
	v_pk_fma_f32 v[134:135], v[134:135], v[236:237], v[78:79]
	v_pk_fma_f32 v[172:173], v[172:173], v[230:231], v[76:77]
	v_pk_fma_f32 v[174:175], v[174:175], v[230:231], v[78:79]
	v_pk_fma_f32 v[136:137], v[136:137], v[236:237], v[80:81]
	v_pk_fma_f32 v[138:139], v[138:139], v[236:237], v[82:83]
	v_pk_fma_f32 v[176:177], v[176:177], v[230:231], v[80:81]
	v_pk_fma_f32 v[178:179], v[178:179], v[230:231], v[82:83]
	v_pk_fma_f32 v[140:141], v[140:141], v[236:237], v[84:85]
	v_pk_fma_f32 v[142:143], v[142:143], v[236:237], v[86:87]
	v_pk_fma_f32 v[180:181], v[180:181], v[230:231], v[84:85]
	v_pk_fma_f32 v[182:183], v[182:183], v[230:231], v[86:87]
	v_exp_f32_e32 v108, v108
	v_exp_f32_e32 v109, v109
	v_exp_f32_e32 v110, v110
	v_exp_f32_e32 v111, v111
	v_exp_f32_e32 v148, v148
	v_exp_f32_e32 v149, v149
	v_exp_f32_e32 v150, v150
	v_exp_f32_e32 v151, v151
	v_exp_f32_e32 v112, v112
	v_exp_f32_e32 v113, v113
	v_exp_f32_e32 v114, v114
	v_exp_f32_e32 v115, v115
	v_exp_f32_e32 v152, v152
	v_exp_f32_e32 v153, v153
	v_exp_f32_e32 v154, v154
	v_exp_f32_e32 v155, v155
	v_exp_f32_e32 v116, v116
	v_exp_f32_e32 v117, v117
	v_exp_f32_e32 v118, v118
	v_exp_f32_e32 v119, v119
	v_exp_f32_e32 v156, v156
	v_exp_f32_e32 v157, v157
	v_exp_f32_e32 v158, v158
	v_exp_f32_e32 v159, v159
	v_exp_f32_e32 v120, v120
	v_exp_f32_e32 v121, v121
	v_exp_f32_e32 v122, v122
	v_exp_f32_e32 v123, v123
	v_exp_f32_e32 v160, v160
	v_exp_f32_e32 v161, v161
	v_exp_f32_e32 v162, v162
	v_exp_f32_e32 v163, v163
	v_exp_f32_e32 v124, v124
	v_exp_f32_e32 v125, v125
	v_exp_f32_e32 v126, v126
	v_exp_f32_e32 v127, v127
	v_exp_f32_e32 v164, v164
	v_exp_f32_e32 v165, v165
	v_exp_f32_e32 v166, v166
	v_exp_f32_e32 v167, v167
	v_exp_f32_e32 v128, v128
	v_exp_f32_e32 v129, v129
	v_exp_f32_e32 v130, v130
	v_exp_f32_e32 v131, v131
	v_exp_f32_e32 v168, v168
	v_exp_f32_e32 v169, v169
	v_exp_f32_e32 v170, v170
	v_exp_f32_e32 v171, v171
	v_exp_f32_e32 v132, v132
	v_exp_f32_e32 v133, v133
	v_exp_f32_e32 v134, v134
	v_exp_f32_e32 v135, v135
	v_exp_f32_e32 v172, v172
	v_exp_f32_e32 v173, v173
	v_exp_f32_e32 v174, v174
	v_exp_f32_e32 v175, v175
	v_exp_f32_e32 v136, v136
	v_exp_f32_e32 v137, v137
	v_exp_f32_e32 v138, v138
	v_exp_f32_e32 v139, v139
	v_exp_f32_e32 v176, v176
	v_exp_f32_e32 v177, v177
	v_exp_f32_e32 v178, v178
	v_exp_f32_e32 v179, v179
	v_exp_f32_e32 v140, v140
	v_exp_f32_e32 v141, v141
	v_exp_f32_e32 v142, v142
	v_exp_f32_e32 v143, v143
	v_exp_f32_e32 v180, v180
	v_exp_f32_e32 v181, v181
	v_exp_f32_e32 v182, v182
	v_exp_f32_e32 v183, v183
	s_cmp_lg_u32 s36, 0
	s_cbranch_scc1 .Lat_m2
	v_mov_b32_e32 v108, 0
	v_mov_b32_e32 v109, 0
	v_mov_b32_e32 v110, 0
	v_mov_b32_e32 v111, 0
	v_mov_b32_e32 v112, 0
	v_mov_b32_e32 v113, 0
	v_mov_b32_e32 v114, 0
	v_mov_b32_e32 v115, 0
	v_mov_b32_e32 v116, 0
	v_mov_b32_e32 v117, 0
	v_mov_b32_e32 v118, 0
	v_mov_b32_e32 v119, 0
	v_mov_b32_e32 v120, 0
	v_mov_b32_e32 v121, 0
	v_mov_b32_e32 v122, 0
	v_mov_b32_e32 v123, 0
	v_mov_b32_e32 v148, 0
	v_mov_b32_e32 v149, 0
	v_mov_b32_e32 v150, 0
	v_mov_b32_e32 v151, 0
	v_mov_b32_e32 v152, 0
	v_mov_b32_e32 v153, 0
	v_mov_b32_e32 v154, 0
	v_mov_b32_e32 v155, 0
	v_mov_b32_e32 v156, 0
	v_mov_b32_e32 v157, 0
	v_mov_b32_e32 v158, 0
	v_mov_b32_e32 v159, 0
.Lat_m2:
	s_nop 0
	v_pk_add_f32 v[232:233], v[108:109], v[110:111]
	v_pk_add_f32 v[234:235], v[112:113], v[114:115]
	v_pk_add_f32 v[226:227], v[148:149], v[150:151]
	v_pk_add_f32 v[228:229], v[152:153], v[154:155]
	v_pk_add_f32 v[232:233], v[232:233], v[116:117]
	v_pk_add_f32 v[234:235], v[234:235], v[118:119]
	v_pk_add_f32 v[226:227], v[226:227], v[156:157]
	v_pk_add_f32 v[228:229], v[228:229], v[158:159]
	v_pk_add_f32 v[232:233], v[232:233], v[120:121]
	v_pk_add_f32 v[234:235], v[234:235], v[122:123]
	v_pk_add_f32 v[226:227], v[226:227], v[160:161]
	v_pk_add_f32 v[228:229], v[228:229], v[162:163]
	v_pk_add_f32 v[232:233], v[232:233], v[124:125]
	v_pk_add_f32 v[234:235], v[234:235], v[126:127]
	v_pk_add_f32 v[226:227], v[226:227], v[164:165]
	v_pk_add_f32 v[228:229], v[228:229], v[166:167]
	v_pk_add_f32 v[232:233], v[232:233], v[128:129]
	v_pk_add_f32 v[234:235], v[234:235], v[130:131]
	v_pk_add_f32 v[226:227], v[226:227], v[168:169]
	v_pk_add_f32 v[228:229], v[228:229], v[170:171]
	v_pk_add_f32 v[232:233], v[232:233], v[132:133]
	v_pk_add_f32 v[234:235], v[234:235], v[134:135]
	v_pk_add_f32 v[226:227], v[226:227], v[172:173]
	v_pk_add_f32 v[228:229], v[228:229], v[174:175]
	v_pk_add_f32 v[232:233], v[232:233], v[136:137]
	v_pk_add_f32 v[234:235], v[234:235], v[138:139]
	v_pk_add_f32 v[226:227], v[226:227], v[176:177]
	v_pk_add_f32 v[228:229], v[228:229], v[178:179]
	v_pk_add_f32 v[232:233], v[232:233], v[140:141]
	v_pk_add_f32 v[234:235], v[234:235], v[142:143]
	v_pk_add_f32 v[226:227], v[226:227], v[180:181]
	v_pk_add_f32 v[228:229], v[228:229], v[182:183]
	v_pk_add_f32 v[232:233], v[232:233], v[234:235]
	v_pk_add_f32 v[226:227], v[226:227], v[228:229]
	v_add_f32_e32 v232, v232, v233
	v_add_f32_e32 v226, v226, v227
	v_cvt_pk_bf16_f32 v108, v108, v109
	v_cvt_pk_bf16_f32 v109, v110, v111
	v_cvt_pk_bf16_f32 v110, v112, v113
	v_cvt_pk_bf16_f32 v111, v114, v115
	v_cvt_pk_bf16_f32 v146, v148, v149
	v_cvt_pk_bf16_f32 v147, v150, v151
	v_cvt_pk_bf16_f32 v116, v116, v117
	v_cvt_pk_bf16_f32 v117, v118, v119
	v_cvt_pk_bf16_f32 v118, v120, v121
	v_cvt_pk_bf16_f32 v119, v122, v123
	v_cvt_pk_bf16_f32 v152, v152, v153
	v_cvt_pk_bf16_f32 v153, v154, v155
	v_cvt_pk_bf16_f32 v154, v156, v157
	v_cvt_pk_bf16_f32 v155, v158, v159
	v_cvt_pk_bf16_f32 v124, v124, v125
	v_cvt_pk_bf16_f32 v125, v126, v127
	v_cvt_pk_bf16_f32 v126, v128, v129
	v_cvt_pk_bf16_f32 v127, v130, v131
	v_cvt_pk_bf16_f32 v160, v160, v161
	v_cvt_pk_bf16_f32 v161, v162, v163
	v_cvt_pk_bf16_f32 v162, v164, v165
	v_cvt_pk_bf16_f32 v163, v166, v167
	v_cvt_pk_bf16_f32 v132, v132, v133
	v_cvt_pk_bf16_f32 v133, v134, v135
	v_cvt_pk_bf16_f32 v134, v136, v137
	v_cvt_pk_bf16_f32 v135, v138, v139
	v_cvt_pk_bf16_f32 v168, v168, v169
	v_cvt_pk_bf16_f32 v169, v170, v171
	v_cvt_pk_bf16_f32 v170, v172, v173
	v_cvt_pk_bf16_f32 v171, v174, v175
	v_cvt_pk_bf16_f32 v140, v140, v141
	v_cvt_pk_bf16_f32 v141, v142, v143
	v_mov_b32_e32 v142, 0
	v_mov_b32_e32 v143, 0
	v_cvt_pk_bf16_f32 v176, v176, v177
	v_cvt_pk_bf16_f32 v177, v178, v179
	v_cvt_pk_bf16_f32 v178, v180, v181
	v_cvt_pk_bf16_f32 v179, v182, v183
	ds_bpermute_b32 v233, v15, v232
	ds_bpermute_b32 v227, v15, v226
	s_waitcnt lgkmcnt(2)
	v_mfma_f32_16x16x32_bf16 v[184:187], v[20:23], v[108:111], 0
	v_mfma_f32_16x16x32_bf16 v[188:191], v[24:27], v[108:111], 0
	v_mfma_f32_16x16x32_bf16 v[192:195], v[28:31], v[108:111], 0
	v_mfma_f32_16x16x32_bf16 v[196:199], v[32:35], v[108:111], 0
	v_mfma_f32_16x16x32_bf16 v[200:203], v[20:23], v[144:147], 0
	v_mfma_f32_16x16x32_bf16 v[204:207], v[24:27], v[144:147], 0
	v_mfma_f32_16x16x32_bf16 v[208:211], v[28:31], v[144:147], 0
	v_mfma_f32_16x16x32_bf16 v[212:215], v[32:35], v[144:147], 0
	ds_read2_b64 v[20:23], v11 offset0:32 offset1:36
	ds_read2_b64 v[24:27], v12 offset0:32 offset1:36
	ds_read2_b64 v[28:31], v13 offset0:32 offset1:36
	ds_read2_b64 v[32:35], v14 offset0:32 offset1:36
	v_mfma_f32_16x16x32_bf16 v[184:187], v[36:39], v[116:119], v[184:187]
	v_mfma_f32_16x16x32_bf16 v[188:191], v[40:43], v[116:119], v[188:191]
	v_mfma_f32_16x16x32_bf16 v[192:195], v[44:47], v[116:119], v[192:195]
	v_mfma_f32_16x16x32_bf16 v[196:199], v[48:51], v[116:119], v[196:199]
	v_mfma_f32_16x16x32_bf16 v[200:203], v[36:39], v[152:155], v[200:203]
	v_mfma_f32_16x16x32_bf16 v[204:207], v[40:43], v[152:155], v[204:207]
	v_mfma_f32_16x16x32_bf16 v[208:211], v[44:47], v[152:155], v[208:211]
	v_mfma_f32_16x16x32_bf16 v[212:215], v[48:51], v[152:155], v[212:215]
	ds_read2_b64 v[36:39], v11 offset0:40 offset1:44
	ds_read2_b64 v[40:43], v12 offset0:40 offset1:44
	ds_read2_b64 v[44:47], v13 offset0:40 offset1:44
	ds_read2_b64 v[48:51], v14 offset0:40 offset1:44
	s_waitcnt lgkmcnt(8)
	v_add_f32_e32 v232, v232, v233
	v_add_f32_e32 v226, v226, v227
	s_nop 0
	ds_bpermute_b32 v233, v16, v232
	ds_bpermute_b32 v227, v16, v226
	s_waitcnt lgkmcnt(6)
	v_mfma_f32_16x16x32_bf16 v[184:187], v[20:23], v[124:127], v[184:187]
	v_mfma_f32_16x16x32_bf16 v[188:191], v[24:27], v[124:127], v[188:191]
	v_mfma_f32_16x16x32_bf16 v[192:195], v[28:31], v[124:127], v[192:195]
	v_mfma_f32_16x16x32_bf16 v[196:199], v[32:35], v[124:127], v[196:199]
	v_mfma_f32_16x16x32_bf16 v[200:203], v[20:23], v[160:163], v[200:203]
	v_mfma_f32_16x16x32_bf16 v[204:207], v[24:27], v[160:163], v[204:207]
	v_mfma_f32_16x16x32_bf16 v[208:211], v[28:31], v[160:163], v[208:211]
	v_mfma_f32_16x16x32_bf16 v[212:215], v[32:35], v[160:163], v[212:215]
	ds_read2_b64 v[20:23], v11 offset0:48 offset1:52
	ds_read2_b64 v[24:27], v12 offset0:48 offset1:52
	ds_read2_b64 v[28:31], v13 offset0:48 offset1:52
	ds_read2_b64 v[32:35], v14 offset0:48 offset1:52
	s_waitcnt lgkmcnt(6)
	v_mfma_f32_16x16x32_bf16 v[184:187], v[36:39], v[132:135], v[184:187]
	v_mfma_f32_16x16x32_bf16 v[188:191], v[40:43], v[132:135], v[188:191]
	v_mfma_f32_16x16x32_bf16 v[192:195], v[44:47], v[132:135], v[192:195]
	v_mfma_f32_16x16x32_bf16 v[196:199], v[48:51], v[132:135], v[196:199]
	v_mfma_f32_16x16x32_bf16 v[200:203], v[36:39], v[168:171], v[200:203]
	v_mfma_f32_16x16x32_bf16 v[204:207], v[40:43], v[168:171], v[204:207]
	v_mfma_f32_16x16x32_bf16 v[208:211], v[44:47], v[168:171], v[208:211]
	v_mfma_f32_16x16x32_bf16 v[212:215], v[48:51], v[168:171], v[212:215]
	s_waitcnt lgkmcnt(0)
	v_mfma_f32_16x16x32_bf16 v[184:187], v[20:23], v[140:143], v[184:187]
	v_mfma_f32_16x16x32_bf16 v[188:191], v[24:27], v[140:143], v[188:191]
	v_mfma_f32_16x16x32_bf16 v[192:195], v[28:31], v[140:143], v[192:195]
	v_mfma_f32_16x16x32_bf16 v[196:199], v[32:35], v[140:143], v[196:199]
	v_mfma_f32_16x16x32_bf16 v[200:203], v[20:23], v[176:179], v[200:203]
	v_mfma_f32_16x16x32_bf16 v[204:207], v[24:27], v[176:179], v[204:207]
	v_mfma_f32_16x16x32_bf16 v[208:211], v[28:31], v[176:179], v[208:211]
	v_mfma_f32_16x16x32_bf16 v[212:215], v[32:35], v[176:179], v[212:215]
	v_add_f32_e32 v232, v232, v233
	v_add_f32_e32 v226, v226, v227
	v_add_f32_e32 v232, v232, v88
	v_add_f32_e32 v226, v226, v88
	v_rcp_f32_e32 v236, v232
	v_rcp_f32_e32 v230, v226
	v_mov_b32_e32 v237, v236
	v_mov_b32_e32 v231, v230
	s_nop 1
	v_pk_mul_f32 v[184:185], v[184:185], v[236:237]
	v_pk_mul_f32 v[186:187], v[186:187], v[236:237]
	v_pk_mul_f32 v[188:189], v[188:189], v[236:237]
	v_pk_mul_f32 v[190:191], v[190:191], v[236:237]
	v_pk_mul_f32 v[192:193], v[192:193], v[236:237]
	v_pk_mul_f32 v[194:195], v[194:195], v[236:237]
	v_pk_mul_f32 v[196:197], v[196:197], v[236:237]
	v_pk_mul_f32 v[198:199], v[198:199], v[236:237]
	v_pk_mul_f32 v[200:201], v[200:201], v[230:231]
	v_pk_mul_f32 v[202:203], v[202:203], v[230:231]
	v_pk_mul_f32 v[204:205], v[204:205], v[230:231]
	v_pk_mul_f32 v[206:207], v[206:207], v[230:231]
	v_pk_mul_f32 v[208:209], v[208:209], v[230:231]
	v_pk_mul_f32 v[210:211], v[210:211], v[230:231]
	v_pk_mul_f32 v[212:213], v[212:213], v[230:231]
	v_pk_mul_f32 v[214:215], v[214:215], v[230:231]
	v_cvt_pk_bf16_f32 v184, v184, v185
	v_cvt_pk_bf16_f32 v185, v186, v187
	v_cvt_pk_bf16_f32 v188, v188, v189
	v_cvt_pk_bf16_f32 v189, v190, v191
	v_cvt_pk_bf16_f32 v192, v192, v193
	v_cvt_pk_bf16_f32 v193, v194, v195
	v_cvt_pk_bf16_f32 v196, v196, v197
	v_cvt_pk_bf16_f32 v197, v198, v199
	v_cvt_pk_bf16_f32 v200, v200, v201
	v_cvt_pk_bf16_f32 v201, v202, v203
	v_cvt_pk_bf16_f32 v204, v204, v205
	v_cvt_pk_bf16_f32 v205, v206, v207
	v_cvt_pk_bf16_f32 v208, v208, v209
	v_cvt_pk_bf16_f32 v209, v210, v211
	v_cvt_pk_bf16_f32 v212, v212, v213
	v_cvt_pk_bf16_f32 v213, v214, v215
	global_store_dwordx2 v9, v[184:185], s[50:51] offset:0
	global_store_dwordx2 v9, v[188:189], s[50:51] offset:32
	global_store_dwordx2 v9, v[192:193], s[50:51] offset:64
	global_store_dwordx2 v9, v[196:197], s[50:51] offset:96
	global_store_dwordx2 v9, v[200:201], s[60:61] offset:0
	global_store_dwordx2 v9, v[204:205], s[60:61] offset:32
	global_store_dwordx2 v9, v[208:209], s[60:61] offset:64
	global_store_dwordx2 v9, v[212:213], s[60:61] offset:96
	s_add_u32 s50, s50, 0x20000
	s_addc_u32 s51, s51, 0
	s_add_u32 s60, s60, 0x20000
	s_addc_u32 s61, s61, 0
	ds_read_b128 v[20:23], v10 offset:13824
	ds_read_b128 v[24:27], v10 offset:13888
	ds_read_b128 v[28:31], v10 offset:16128
	ds_read_b128 v[32:35], v10 offset:16192
	ds_read_b128 v[36:39], v10 offset:18432
	ds_read_b128 v[40:43], v10 offset:18496
	ds_read_b128 v[44:47], v10 offset:20736
	ds_read_b128 v[48:51], v10 offset:20800
	ds_read_b128 v[216:219], v10 offset:23040
	ds_read_b128 v[220:223], v10 offset:23104
	s_waitcnt vmcnt(8)
	v_lshlrev_b32_e32 v234, 16, v92
	v_and_b32_e32 v235, 0xffff0000, v92
	v_pk_mul_f32 v[232:233], v[234:235], v[234:235]
	v_lshlrev_b32_e32 v228, 16, v100
	v_and_b32_e32 v229, 0xffff0000, v100
	v_pk_mul_f32 v[226:227], v[228:229], v[228:229]
	v_lshlrev_b32_e32 v234, 16, v93
	v_and_b32_e32 v235, 0xffff0000, v93
	v_pk_fma_f32 v[232:233], v[234:235], v[234:235], v[232:233]
	v_lshlrev_b32_e32 v228, 16, v101
	v_and_b32_e32 v229, 0xffff0000, v101
	v_pk_fma_f32 v[226:227], v[228:229], v[228:229], v[226:227]
	v_lshlrev_b32_e32 v234, 16, v94
	v_and_b32_e32 v235, 0xffff0000, v94
	v_pk_fma_f32 v[232:233], v[234:235], v[234:235], v[232:233]
	v_lshlrev_b32_e32 v228, 16, v102
	v_and_b32_e32 v229, 0xffff0000, v102
	v_pk_fma_f32 v[226:227], v[228:229], v[228:229], v[226:227]
	v_lshlrev_b32_e32 v234, 16, v95
	v_and_b32_e32 v235, 0xffff0000, v95
	v_pk_fma_f32 v[232:233], v[234:235], v[234:235], v[232:233]
	v_lshlrev_b32_e32 v228, 16, v103
	v_and_b32_e32 v229, 0xffff0000, v103
	v_pk_fma_f32 v[226:227], v[228:229], v[228:229], v[226:227]
	v_lshlrev_b32_e32 v234, 16, v96
	v_and_b32_e32 v235, 0xffff0000, v96
	v_pk_fma_f32 v[232:233], v[234:235], v[234:235], v[232:233]
	v_lshlrev_b32_e32 v228, 16, v104
	v_and_b32_e32 v229, 0xffff0000, v104
	v_pk_fma_f32 v[226:227], v[228:229], v[228:229], v[226:227]
	v_lshlrev_b32_e32 v234, 16, v97
	v_and_b32_e32 v235, 0xffff0000, v97
	v_pk_fma_f32 v[232:233], v[234:235], v[234:235], v[232:233]
	v_lshlrev_b32_e32 v228, 16, v105
	v_and_b32_e32 v229, 0xffff0000, v105
	v_pk_fma_f32 v[226:227], v[228:229], v[228:229], v[226:227]
	v_lshlrev_b32_e32 v234, 16, v98
	v_and_b32_e32 v235, 0xffff0000, v98
	v_pk_fma_f32 v[232:233], v[234:235], v[234:235], v[232:233]
	v_lshlrev_b32_e32 v228, 16, v106
	v_and_b32_e32 v229, 0xffff0000, v106
	v_pk_fma_f32 v[226:227], v[228:229], v[228:229], v[226:227]
	v_lshlrev_b32_e32 v234, 16, v99
	v_and_b32_e32 v235, 0xffff0000, v99
	v_pk_fma_f32 v[232:233], v[234:235], v[234:235], v[232:233]
	v_lshlrev_b32_e32 v228, 16, v107
	v_and_b32_e32 v229, 0xffff0000, v107
	v_pk_fma_f32 v[226:227], v[228:229], v[228:229], v[226:227]
	v_add_f32_e32 v232, v232, v233
	v_add_f32_e32 v226, v226, v227
	s_nop 0
	ds_bpermute_b32 v233, v15, v232
	ds_bpermute_b32 v227, v15, v226
	s_waitcnt lgkmcnt(6)
	v_mfma_f32_16x16x32_bf16 v[108:111], v[20:23], v[92:95], 0
	v_mfma_f32_16x16x32_bf16 v[112:115], v[28:31], v[92:95], 0
	v_mfma_f32_16x16x32_bf16 v[148:151], v[28:31], v[100:103], 0
	v_mfma_f32_16x16x32_bf16 v[116:119], v[36:39], v[92:95], 0
	v_mfma_f32_16x16x32_bf16 v[152:155], v[36:39], v[100:103], 0
	v_mfma_f32_16x16x32_bf16 v[108:111], v[24:27], v[96:99], v[108:111]
	v_mfma_f32_16x16x32_bf16 v[112:115], v[32:35], v[96:99], v[112:115]
	v_mfma_f32_16x16x32_bf16 v[148:151], v[32:35], v[104:107], v[148:151]
	v_mfma_f32_16x16x32_bf16 v[116:119], v[40:43], v[96:99], v[116:119]
	v_mfma_f32_16x16x32_bf16 v[152:155], v[40:43], v[104:107], v[152:155]
	ds_read_b128 v[20:23], v10 offset:25344
	ds_read_b128 v[24:27], v10 offset:25408
	ds_read_b128 v[28:31], v10 offset:27648
	ds_read_b128 v[32:35], v10 offset:27712
	ds_read_b128 v[36:39], v10 offset:29952
	ds_read_b128 v[40:43], v10 offset:30016
	s_waitcnt lgkmcnt(6)
	v_add_f32_e32 v232, v232, v233
	v_add_f32_e32 v226, v226, v227
	s_nop 0
	ds_bpermute_b32 v233, v16, v232
	ds_bpermute_b32 v227, v16, v226
	v_mfma_f32_16x16x32_bf16 v[120:123], v[44:47], v[92:95], 0
	v_mfma_f32_16x16x32_bf16 v[156:159], v[44:47], v[100:103], 0
	v_mfma_f32_16x16x32_bf16 v[124:127], v[216:219], v[92:95], 0
	v_mfma_f32_16x16x32_bf16 v[160:163], v[216:219], v[100:103], 0
	v_mfma_f32_16x16x32_bf16 v[120:123], v[48:51], v[96:99], v[120:123]
	v_mfma_f32_16x16x32_bf16 v[156:159], v[48:51], v[104:107], v[156:159]
	v_mfma_f32_16x16x32_bf16 v[124:127], v[220:223], v[96:99], v[124:127]
	v_mfma_f32_16x16x32_bf16 v[160:163], v[220:223], v[104:107], v[160:163]
	ds_read_b128 v[44:47], v10 offset:32256
	ds_read_b128 v[48:51], v10 offset:32320
	ds_read_b128 v[216:219], v10 offset:34560
	ds_read_b128 v[220:223], v10 offset:34624
	s_waitcnt lgkmcnt(6)
	v_mfma_f32_16x16x32_bf16 v[128:131], v[20:23], v[92:95], 0
	v_mfma_f32_16x16x32_bf16 v[164:167], v[20:23], v[100:103], 0
	v_mfma_f32_16x16x32_bf16 v[132:135], v[28:31], v[92:95], 0
	v_mfma_f32_16x16x32_bf16 v[168:171], v[28:31], v[100:103], 0
	v_mfma_f32_16x16x32_bf16 v[136:139], v[36:39], v[92:95], 0
	v_mfma_f32_16x16x32_bf16 v[172:175], v[36:39], v[100:103], 0
	v_mfma_f32_16x16x32_bf16 v[128:131], v[24:27], v[96:99], v[128:131]
	v_mfma_f32_16x16x32_bf16 v[164:167], v[24:27], v[104:107], v[164:167]
	v_mfma_f32_16x16x32_bf16 v[132:135], v[32:35], v[96:99], v[132:135]
	v_mfma_f32_16x16x32_bf16 v[168:171], v[32:35], v[104:107], v[168:171]
	v_mfma_f32_16x16x32_bf16 v[136:139], v[40:43], v[96:99], v[136:139]
	v_mfma_f32_16x16x32_bf16 v[172:175], v[40:43], v[104:107], v[172:175]
	s_waitcnt lgkmcnt(0)
	v_mfma_f32_16x16x32_bf16 v[140:143], v[44:47], v[92:95], 0
	v_mfma_f32_16x16x32_bf16 v[176:179], v[44:47], v[100:103], 0
	v_mfma_f32_16x16x32_bf16 v[180:183], v[216:219], v[100:103], 0
	v_mfma_f32_16x16x32_bf16 v[140:143], v[48:51], v[96:99], v[140:143]
	v_mfma_f32_16x16x32_bf16 v[176:179], v[48:51], v[104:107], v[176:179]
	v_mfma_f32_16x16x32_bf16 v[180:183], v[220:223], v[104:107], v[180:183]
	s_cmpk_gt_u32 s39, 0x3ff
	s_cbranch_scc1 .Lat_nopfk
	s_and_b32 s3, s39, 3
	s_bfe_u32 s4, s39, 0x70002
	s_lshr_b32 s5, s39, 9
	s_lshl_b32 s6, s5, 14
	s_lshl_b32 s7, s4, 7
	s_add_i32 s6, s6, s7
	s_sub_i32 s6, s6, 0x80
	s_mul_i32 s7, s6, 0x1400
	s_ashr_i32 s9, s7, 31
	s_add_u32 s40, s14, s7
	s_addc_u32 s41, s15, s9
	s_lshl_b32 s7, s3, 7
	s_add_u32 s40, s40, s7
	s_addc_u32 s41, s41, 0
	s_lshl_b32 s6, s5, 2
	s_add_i32 s6, s6, s3
	s_lshl_b32 s6, s6, 21
	s_lshl_b32 s7, s4, 8
	s_sub_i32 s7, s7, 0x100
	s_add_i32 s6, s6, s7
	s_ashr_i32 s7, s6, 31
	s_add_u32 s42, s16, s6
	s_addc_u32 s43, s17, s7
	global_load_dwordx4 v[92:95], v6, s[40:41] offset:0
	global_load_dwordx4 v[96:99], v6, s[40:41] offset:16
	global_load_dwordx4 v[100:103], v6, s[40:41] offset:32
	global_load_dwordx4 v[104:107], v6, s[40:41] offset:48
.Lat_nopfk:
	ds_read2_b64 v[20:23], v11 offset0:24 offset1:28
	ds_read2_b64 v[24:27], v12 offset0:24 offset1:28
	ds_read2_b64 v[28:31], v13 offset0:24 offset1:28
	ds_read2_b64 v[32:35], v14 offset0:24 offset1:28
	ds_read2_b64 v[36:39], v11 offset0:32 offset1:36
	ds_read2_b64 v[40:43], v12 offset0:32 offset1:36
	ds_read2_b64 v[44:47], v13 offset0:32 offset1:36
	ds_read2_b64 v[48:51], v14 offset0:32 offset1:36
	v_add_f32_e32 v232, v232, v233
	v_add_f32_e32 v226, v226, v227
	v_mul_f32_e32 v232, 0x3c800000, v232
	v_mul_f32_e32 v226, 0x3c800000, v226
	v_add_f32_e32 v232, 0x358637bd, v232
	v_add_f32_e32 v226, 0x358637bd, v226
	v_rsq_f32_e32 v236, v232
	v_rsq_f32_e32 v230, v226
	v_mov_b32_e32 v237, v236
	v_mov_b32_e32 v231, v230
	s_nop 1
	v_pk_fma_f32 v[108:109], v[108:109], v[236:237], v[52:53]
	v_pk_fma_f32 v[110:111], v[110:111], v[236:237], v[54:55]
	v_pk_fma_f32 v[148:149], v[148:149], v[230:231], v[52:53]
	v_pk_fma_f32 v[150:151], v[150:151], v[230:231], v[54:55]
	v_pk_fma_f32 v[112:113], v[112:113], v[236:237], v[56:57]
	v_pk_fma_f32 v[114:115], v[114:115], v[236:237], v[58:59]
	v_pk_fma_f32 v[152:153], v[152:153], v[230:231], v[56:57]
	v_pk_fma_f32 v[154:155], v[154:155], v[230:231], v[58:59]
	v_pk_fma_f32 v[116:117], v[116:117], v[236:237], v[60:61]
	v_pk_fma_f32 v[118:119], v[118:119], v[236:237], v[62:63]
	v_pk_fma_f32 v[156:157], v[156:157], v[230:231], v[60:61]
	v_pk_fma_f32 v[158:159], v[158:159], v[230:231], v[62:63]
	v_pk_fma_f32 v[120:121], v[120:121], v[236:237], v[64:65]
	v_pk_fma_f32 v[122:123], v[122:123], v[236:237], v[66:67]
	v_pk_fma_f32 v[160:161], v[160:161], v[230:231], v[64:65]
	v_pk_fma_f32 v[162:163], v[162:163], v[230:231], v[66:67]
	v_pk_fma_f32 v[124:125], v[124:125], v[236:237], v[68:69]
	v_pk_fma_f32 v[126:127], v[126:127], v[236:237], v[70:71]
	v_pk_fma_f32 v[164:165], v[164:165], v[230:231], v[68:69]
	v_pk_fma_f32 v[166:167], v[166:167], v[230:231], v[70:71]
	v_pk_fma_f32 v[128:129], v[128:129], v[236:237], v[72:73]
	v_pk_fma_f32 v[130:131], v[130:131], v[236:237], v[74:75]
	v_pk_fma_f32 v[168:169], v[168:169], v[230:231], v[72:73]
	v_pk_fma_f32 v[170:171], v[170:171], v[230:231], v[74:75]
	v_pk_fma_f32 v[132:133], v[132:133], v[236:237], v[76:77]
	v_pk_fma_f32 v[134:135], v[134:135], v[236:237], v[78:79]
	v_pk_fma_f32 v[172:173], v[172:173], v[230:231], v[76:77]
	v_pk_fma_f32 v[174:175], v[174:175], v[230:231], v[78:79]
	v_pk_fma_f32 v[136:137], v[136:137], v[236:237], v[80:81]
	v_pk_fma_f32 v[138:139], v[138:139], v[236:237], v[82:83]
	v_pk_fma_f32 v[176:177], v[176:177], v[230:231], v[80:81]
	v_pk_fma_f32 v[178:179], v[178:179], v[230:231], v[82:83]
	v_pk_fma_f32 v[140:141], v[140:141], v[236:237], v[84:85]
	v_pk_fma_f32 v[142:143], v[142:143], v[236:237], v[86:87]
	v_pk_fma_f32 v[180:181], v[180:181], v[230:231], v[84:85]
	v_pk_fma_f32 v[182:183], v[182:183], v[230:231], v[86:87]
	v_exp_f32_e32 v108, v108
	v_exp_f32_e32 v109, v109
	v_exp_f32_e32 v110, v110
	v_exp_f32_e32 v111, v111
	v_exp_f32_e32 v148, v148
	v_exp_f32_e32 v149, v149
	v_exp_f32_e32 v150, v150
	v_exp_f32_e32 v151, v151
	v_exp_f32_e32 v112, v112
	v_exp_f32_e32 v113, v113
	v_exp_f32_e32 v114, v114
	v_exp_f32_e32 v115, v115
	v_exp_f32_e32 v152, v152
	v_exp_f32_e32 v153, v153
	v_exp_f32_e32 v154, v154
	v_exp_f32_e32 v155, v155
	v_exp_f32_e32 v116, v116
	v_exp_f32_e32 v117, v117
	v_exp_f32_e32 v118, v118
	v_exp_f32_e32 v119, v119
	v_exp_f32_e32 v156, v156
	v_exp_f32_e32 v157, v157
	v_exp_f32_e32 v158, v158
	v_exp_f32_e32 v159, v159
	v_exp_f32_e32 v120, v120
	v_exp_f32_e32 v121, v121
	v_exp_f32_e32 v122, v122
	v_exp_f32_e32 v123, v123
	v_exp_f32_e32 v160, v160
	v_exp_f32_e32 v161, v161
	v_exp_f32_e32 v162, v162
	v_exp_f32_e32 v163, v163
	v_exp_f32_e32 v124, v124
	v_exp_f32_e32 v125, v125
	v_exp_f32_e32 v126, v126
	v_exp_f32_e32 v127, v127
	v_exp_f32_e32 v164, v164
	v_exp_f32_e32 v165, v165
	v_exp_f32_e32 v166, v166
	v_exp_f32_e32 v167, v167
	v_exp_f32_e32 v128, v128
	v_exp_f32_e32 v129, v129
	v_exp_f32_e32 v130, v130
	v_exp_f32_e32 v131, v131
	v_exp_f32_e32 v168, v168
	v_exp_f32_e32 v169, v169
	v_exp_f32_e32 v170, v170
	v_exp_f32_e32 v171, v171
	v_exp_f32_e32 v132, v132
	v_exp_f32_e32 v133, v133
	v_exp_f32_e32 v134, v134
	v_exp_f32_e32 v135, v135
	v_exp_f32_e32 v172, v172
	v_exp_f32_e32 v173, v173
	v_exp_f32_e32 v174, v174
	v_exp_f32_e32 v175, v175
	v_exp_f32_e32 v136, v136
	v_exp_f32_e32 v137, v137
	v_exp_f32_e32 v138, v138
	v_exp_f32_e32 v139, v139
	v_exp_f32_e32 v176, v176
	v_exp_f32_e32 v177, v177
	v_exp_f32_e32 v178, v178
	v_exp_f32_e32 v179, v179
	v_exp_f32_e32 v140, v140
	v_exp_f32_e32 v141, v141
	v_exp_f32_e32 v142, v142
	v_exp_f32_e32 v143, v143
	v_exp_f32_e32 v180, v180
	v_exp_f32_e32 v181, v181
	v_exp_f32_e32 v182, v182
	v_exp_f32_e32 v183, v183
	s_cmp_lg_u32 s36, 0
	s_cbranch_scc1 .Lat_m3
	v_mov_b32_e32 v108, 0
	v_mov_b32_e32 v109, 0
	v_mov_b32_e32 v110, 0
	v_mov_b32_e32 v111, 0
	v_mov_b32_e32 v112, 0
	v_mov_b32_e32 v113, 0
	v_mov_b32_e32 v114, 0
	v_mov_b32_e32 v115, 0
	v_mov_b32_e32 v148, 0
	v_mov_b32_e32 v149, 0
	v_mov_b32_e32 v150, 0
	v_mov_b32_e32 v151, 0
.Lat_m3:
	s_nop 0
	v_pk_add_f32 v[232:233], v[108:109], v[110:111]
	v_pk_add_f32 v[234:235], v[112:113], v[114:115]
	v_pk_add_f32 v[226:227], v[148:149], v[150:151]
	v_pk_add_f32 v[228:229], v[152:153], v[154:155]
	v_pk_add_f32 v[232:233], v[232:233], v[116:117]
	v_pk_add_f32 v[234:235], v[234:235], v[118:119]
	v_pk_add_f32 v[226:227], v[226:227], v[156:157]
	v_pk_add_f32 v[228:229], v[228:229], v[158:159]
	v_pk_add_f32 v[232:233], v[232:233], v[120:121]
	v_pk_add_f32 v[234:235], v[234:235], v[122:123]
	v_pk_add_f32 v[226:227], v[226:227], v[160:161]
	v_pk_add_f32 v[228:229], v[228:229], v[162:163]
	v_pk_add_f32 v[232:233], v[232:233], v[124:125]
	v_pk_add_f32 v[234:235], v[234:235], v[126:127]
	v_pk_add_f32 v[226:227], v[226:227], v[164:165]
	v_pk_add_f32 v[228:229], v[228:229], v[166:167]
	v_pk_add_f32 v[232:233], v[232:233], v[128:129]
	v_pk_add_f32 v[234:235], v[234:235], v[130:131]
	v_pk_add_f32 v[226:227], v[226:227], v[168:169]
	v_pk_add_f32 v[228:229], v[228:229], v[170:171]
	v_pk_add_f32 v[232:233], v[232:233], v[132:133]
	v_pk_add_f32 v[234:235], v[234:235], v[134:135]
	v_pk_add_f32 v[226:227], v[226:227], v[172:173]
	v_pk_add_f32 v[228:229], v[228:229], v[174:175]
	v_pk_add_f32 v[232:233], v[232:233], v[136:137]
	v_pk_add_f32 v[234:235], v[234:235], v[138:139]
	v_pk_add_f32 v[226:227], v[226:227], v[176:177]
	v_pk_add_f32 v[228:229], v[228:229], v[178:179]
	v_pk_add_f32 v[232:233], v[232:233], v[140:141]
	v_pk_add_f32 v[234:235], v[234:235], v[142:143]
	v_pk_add_f32 v[226:227], v[226:227], v[180:181]
	v_pk_add_f32 v[228:229], v[228:229], v[182:183]
	v_pk_add_f32 v[232:233], v[232:233], v[234:235]
	v_pk_add_f32 v[226:227], v[226:227], v[228:229]
	v_add_f32_e32 v232, v232, v233
	v_add_f32_e32 v226, v226, v227
	v_cvt_pk_bf16_f32 v108, v108, v109
	v_cvt_pk_bf16_f32 v109, v110, v111
	v_cvt_pk_bf16_f32 v110, v112, v113
	v_cvt_pk_bf16_f32 v111, v114, v115
	v_cvt_pk_bf16_f32 v146, v148, v149
	v_cvt_pk_bf16_f32 v147, v150, v151
	v_cvt_pk_bf16_f32 v116, v116, v117
	v_cvt_pk_bf16_f32 v117, v118, v119
	v_cvt_pk_bf16_f32 v118, v120, v121
	v_cvt_pk_bf16_f32 v119, v122, v123
	v_cvt_pk_bf16_f32 v152, v152, v153
	v_cvt_pk_bf16_f32 v153, v154, v155
	v_cvt_pk_bf16_f32 v154, v156, v157
	v_cvt_pk_bf16_f32 v155, v158, v159
	v_cvt_pk_bf16_f32 v124, v124, v125
	v_cvt_pk_bf16_f32 v125, v126, v127
	v_cvt_pk_bf16_f32 v126, v128, v129
	v_cvt_pk_bf16_f32 v127, v130, v131
	v_cvt_pk_bf16_f32 v160, v160, v161
	v_cvt_pk_bf16_f32 v161, v162, v163
	v_cvt_pk_bf16_f32 v162, v164, v165
	v_cvt_pk_bf16_f32 v163, v166, v167
	v_cvt_pk_bf16_f32 v132, v132, v133
	v_cvt_pk_bf16_f32 v133, v134, v135
	v_cvt_pk_bf16_f32 v134, v136, v137
	v_cvt_pk_bf16_f32 v135, v138, v139
	v_cvt_pk_bf16_f32 v168, v168, v169
	v_cvt_pk_bf16_f32 v169, v170, v171
	v_cvt_pk_bf16_f32 v170, v172, v173
	v_cvt_pk_bf16_f32 v171, v174, v175
	v_cvt_pk_bf16_f32 v140, v140, v141
	v_cvt_pk_bf16_f32 v141, v142, v143
	v_mov_b32_e32 v142, 0
	v_mov_b32_e32 v143, 0
	v_cvt_pk_bf16_f32 v176, v176, v177
	v_cvt_pk_bf16_f32 v177, v178, v179
	v_cvt_pk_bf16_f32 v178, v180, v181
	v_cvt_pk_bf16_f32 v179, v182, v183
	ds_bpermute_b32 v233, v15, v232
	ds_bpermute_b32 v227, v15, v226
	s_cmpk_gt_u32 s39, 0x3ff
	s_cbranch_scc1 .Lat_nopfv
	global_load_dwordx4 v[112:115], v7, s[42:43] offset:0
	global_load_dwordx4 v[120:123], v7, s[42:43] offset:128
	global_load_dwordx4 v[128:131], v7, s[42:43] offset:256
	global_load_dwordx4 v[136:139], v7, s[42:43] offset:384
.Lat_nopfv:
	s_waitcnt lgkmcnt(2)
	v_mfma_f32_16x16x32_bf16 v[184:187], v[20:23], v[108:111], 0
	v_mfma_f32_16x16x32_bf16 v[188:191], v[24:27], v[108:111], 0
	v_mfma_f32_16x16x32_bf16 v[192:195], v[28:31], v[108:111], 0
	v_mfma_f32_16x16x32_bf16 v[196:199], v[32:35], v[108:111], 0
	v_mfma_f32_16x16x32_bf16 v[200:203], v[20:23], v[144:147], 0
	v_mfma_f32_16x16x32_bf16 v[204:207], v[24:27], v[144:147], 0
	v_mfma_f32_16x16x32_bf16 v[208:211], v[28:31], v[144:147], 0
	v_mfma_f32_16x16x32_bf16 v[212:215], v[32:35], v[144:147], 0
	ds_read2_b64 v[20:23], v11 offset0:40 offset1:44
	ds_read2_b64 v[24:27], v12 offset0:40 offset1:44
	ds_read2_b64 v[28:31], v13 offset0:40 offset1:44
	ds_read2_b64 v[32:35], v14 offset0:40 offset1:44
	v_mfma_f32_16x16x32_bf16 v[184:187], v[36:39], v[116:119], v[184:187]
	v_mfma_f32_16x16x32_bf16 v[188:191], v[40:43], v[116:119], v[188:191]
	v_mfma_f32_16x16x32_bf16 v[192:195], v[44:47], v[116:119], v[192:195]
	v_mfma_f32_16x16x32_bf16 v[196:199], v[48:51], v[116:119], v[196:199]
	v_mfma_f32_16x16x32_bf16 v[200:203], v[36:39], v[152:155], v[200:203]
	v_mfma_f32_16x16x32_bf16 v[204:207], v[40:43], v[152:155], v[204:207]
	v_mfma_f32_16x16x32_bf16 v[208:211], v[44:47], v[152:155], v[208:211]
	v_mfma_f32_16x16x32_bf16 v[212:215], v[48:51], v[152:155], v[212:215]
	ds_read2_b64 v[36:39], v11 offset0:48 offset1:52
	ds_read2_b64 v[40:43], v12 offset0:48 offset1:52
	ds_read2_b64 v[44:47], v13 offset0:48 offset1:52
	ds_read2_b64 v[48:51], v14 offset0:48 offset1:52
	s_waitcnt lgkmcnt(8)
	v_add_f32_e32 v232, v232, v233
	v_add_f32_e32 v226, v226, v227
	s_nop 0
	ds_bpermute_b32 v233, v16, v232
	ds_bpermute_b32 v227, v16, v226
	s_waitcnt lgkmcnt(6)
	v_mfma_f32_16x16x32_bf16 v[184:187], v[20:23], v[124:127], v[184:187]
	v_mfma_f32_16x16x32_bf16 v[188:191], v[24:27], v[124:127], v[188:191]
	v_mfma_f32_16x16x32_bf16 v[192:195], v[28:31], v[124:127], v[192:195]
	v_mfma_f32_16x16x32_bf16 v[196:199], v[32:35], v[124:127], v[196:199]
	v_mfma_f32_16x16x32_bf16 v[200:203], v[20:23], v[160:163], v[200:203]
	v_mfma_f32_16x16x32_bf16 v[204:207], v[24:27], v[160:163], v[204:207]
	v_mfma_f32_16x16x32_bf16 v[208:211], v[28:31], v[160:163], v[208:211]
	v_mfma_f32_16x16x32_bf16 v[212:215], v[32:35], v[160:163], v[212:215]
	ds_read2_b64 v[20:23], v11 offset0:56 offset1:60
	ds_read2_b64 v[24:27], v12 offset0:56 offset1:60
	ds_read2_b64 v[28:31], v13 offset0:56 offset1:60
	ds_read2_b64 v[32:35], v14 offset0:56 offset1:60
	s_waitcnt lgkmcnt(6)
	v_mfma_f32_16x16x32_bf16 v[184:187], v[36:39], v[132:135], v[184:187]
	v_mfma_f32_16x16x32_bf16 v[188:191], v[40:43], v[132:135], v[188:191]
	v_mfma_f32_16x16x32_bf16 v[192:195], v[44:47], v[132:135], v[192:195]
	v_mfma_f32_16x16x32_bf16 v[196:199], v[48:51], v[132:135], v[196:199]
	v_mfma_f32_16x16x32_bf16 v[200:203], v[36:39], v[168:171], v[200:203]
	v_mfma_f32_16x16x32_bf16 v[204:207], v[40:43], v[168:171], v[204:207]
	v_mfma_f32_16x16x32_bf16 v[208:211], v[44:47], v[168:171], v[208:211]
	v_mfma_f32_16x16x32_bf16 v[212:215], v[48:51], v[168:171], v[212:215]
	s_waitcnt lgkmcnt(0)
	v_mfma_f32_16x16x32_bf16 v[184:187], v[20:23], v[140:143], v[184:187]
	v_mfma_f32_16x16x32_bf16 v[188:191], v[24:27], v[140:143], v[188:191]
	v_mfma_f32_16x16x32_bf16 v[192:195], v[28:31], v[140:143], v[192:195]
	v_mfma_f32_16x16x32_bf16 v[196:199], v[32:35], v[140:143], v[196:199]
	v_mfma_f32_16x16x32_bf16 v[200:203], v[20:23], v[176:179], v[200:203]
	v_mfma_f32_16x16x32_bf16 v[204:207], v[24:27], v[176:179], v[204:207]
	v_mfma_f32_16x16x32_bf16 v[208:211], v[28:31], v[176:179], v[208:211]
	v_mfma_f32_16x16x32_bf16 v[212:215], v[32:35], v[176:179], v[212:215]
	v_add_f32_e32 v232, v232, v233
	v_add_f32_e32 v226, v226, v227
	v_add_f32_e32 v232, v232, v88
	v_add_f32_e32 v226, v226, v88
	v_rcp_f32_e32 v236, v232
	v_rcp_f32_e32 v230, v226
	v_mov_b32_e32 v237, v236
	v_mov_b32_e32 v231, v230
	s_nop 1
	v_pk_mul_f32 v[184:185], v[184:185], v[236:237]
	v_pk_mul_f32 v[186:187], v[186:187], v[236:237]
	v_pk_mul_f32 v[188:189], v[188:189], v[236:237]
	v_pk_mul_f32 v[190:191], v[190:191], v[236:237]
	v_pk_mul_f32 v[192:193], v[192:193], v[236:237]
	v_pk_mul_f32 v[194:195], v[194:195], v[236:237]
	v_pk_mul_f32 v[196:197], v[196:197], v[236:237]
	v_pk_mul_f32 v[198:199], v[198:199], v[236:237]
	v_pk_mul_f32 v[200:201], v[200:201], v[230:231]
	v_pk_mul_f32 v[202:203], v[202:203], v[230:231]
	v_pk_mul_f32 v[204:205], v[204:205], v[230:231]
	v_pk_mul_f32 v[206:207], v[206:207], v[230:231]
	v_pk_mul_f32 v[208:209], v[208:209], v[230:231]
	v_pk_mul_f32 v[210:211], v[210:211], v[230:231]
	v_pk_mul_f32 v[212:213], v[212:213], v[230:231]
	v_pk_mul_f32 v[214:215], v[214:215], v[230:231]
	v_cvt_pk_bf16_f32 v184, v184, v185
	v_cvt_pk_bf16_f32 v185, v186, v187
	v_cvt_pk_bf16_f32 v188, v188, v189
	v_cvt_pk_bf16_f32 v189, v190, v191
	v_cvt_pk_bf16_f32 v192, v192, v193
	v_cvt_pk_bf16_f32 v193, v194, v195
	v_cvt_pk_bf16_f32 v196, v196, v197
	v_cvt_pk_bf16_f32 v197, v198, v199
	v_cvt_pk_bf16_f32 v200, v200, v201
	v_cvt_pk_bf16_f32 v201, v202, v203
	v_cvt_pk_bf16_f32 v204, v204, v205
	v_cvt_pk_bf16_f32 v205, v206, v207
	v_cvt_pk_bf16_f32 v208, v208, v209
	v_cvt_pk_bf16_f32 v209, v210, v211
	v_cvt_pk_bf16_f32 v212, v212, v213
	v_cvt_pk_bf16_f32 v213, v214, v215
	global_store_dwordx2 v9, v[184:185], s[50:51] offset:0
	global_store_dwordx2 v9, v[188:189], s[50:51] offset:32
	global_store_dwordx2 v9, v[192:193], s[50:51] offset:64
	global_store_dwordx2 v9, v[196:197], s[50:51] offset:96
	global_store_dwordx2 v9, v[200:201], s[60:61] offset:0
	global_store_dwordx2 v9, v[204:205], s[60:61] offset:32
	global_store_dwordx2 v9, v[208:209], s[60:61] offset:64
	global_store_dwordx2 v9, v[212:213], s[60:61] offset:96
	s_mov_b32 s34, s39
	s_cmpk_gt_u32 s34, 0x3ff
	s_cbranch_scc0 .Lat_item
